# edge pass (ELL atomics) moved to loader waves behind the priming loads; line-aligned A windows; hand-written loader/compute loops
# speedup vs baseline: 1.0155x; 1.0141x over previous
.LBB1_235:
	v_mov_b32_e32 v110, v18
	v_mov_b32_e32 v111, v19
	v_mov_b32_e32 v112, v20
	v_mov_b32_e32 v113, v21
	s_mov_b32 s72, 0x2000
	s_mov_b32 s73, 0
	s_mov_b32 s74, 0x20000
	s_mov_b32 s75, 0
	v_lshl_add_u64 v[158:159], v[158:159], 0, s[74:75]
	v_mul_u32_u24_e32 v163, 0x110, v160
	v_lshl_add_u32 v162, v1, 4, v163
	global_load_dwordx4 v[94:97], v[158:159], off
	v_lshl_add_u64 v[158:159], v[158:159], 0, s[72:73]
	global_load_dwordx4 v[98:101], v[158:159], off
	v_lshl_add_u64 v[158:159], v[158:159], 0, s[72:73]
	global_load_dwordx4 v[102:105], v[158:159], off
	v_lshl_add_u64 v[158:159], v[158:159], 0, s[72:73]
	global_load_dwordx4 v[106:109], v[158:159], off
	v_lshl_add_u64 v[158:159], v[158:159], 0, s[72:73]
	global_load_dwordx4 v[142:145], v[158:159], off
	v_lshl_add_u64 v[158:159], v[158:159], 0, s[72:73]
	global_load_dwordx4 v[146:149], v[158:159], off
	v_lshl_add_u64 v[158:159], v[158:159], 0, s[72:73]
	global_load_dwordx4 v[150:153], v[158:159], off
	v_lshl_add_u64 v[158:159], v[158:159], 0, s[72:73]
	global_load_dwordx4 v[154:157], v[158:159], off
	v_lshl_add_u64 v[158:159], v[158:159], 0, s[72:73]
	s_waitcnt lgkmcnt(0)
	s_barrier
	ds_read_b128 v[114:117], v162 offset:0
	ds_read_b128 v[118:121], v162 offset:8704
	ds_read_b128 v[122:125], v162 offset:32
	ds_read_b128 v[126:129], v162 offset:8736
	ds_read_b128 v[130:133], v162 offset:64
	ds_read_b128 v[134:137], v162 offset:8768
	s_waitcnt lgkmcnt(5)
	v_mfma_f32_32x32x16_f16 v[2:17], v[114:117], v[110:113], 0
	s_waitcnt lgkmcnt(4)
	v_mfma_f32_32x32x16_f16 v[18:33], v[118:121], v[110:113], 0
	ds_read_b128 v[114:117], v162 offset:96
	ds_read_b128 v[118:121], v162 offset:8800
	global_load_dwordx4 v[110:113], v[158:159], off
	v_lshl_add_u64 v[158:159], v[158:159], 0, s[72:73]
	s_waitcnt lgkmcnt(5)
	v_mfma_f32_32x32x16_f16 v[2:17], v[122:125], v[90:93], v[2:17]
	s_waitcnt lgkmcnt(4)
	v_mfma_f32_32x32x16_f16 v[18:33], v[126:129], v[90:93], v[18:33]
	ds_read_b128 v[122:125], v162 offset:128
	ds_read_b128 v[126:129], v162 offset:8832
	global_load_dwordx4 v[90:93], v[158:159], off
	v_lshl_add_u64 v[158:159], v[158:159], 0, s[72:73]
	s_waitcnt lgkmcnt(5)
	v_mfma_f32_32x32x16_f16 v[2:17], v[130:133], v[86:89], v[2:17]
	s_waitcnt lgkmcnt(4)
	v_mfma_f32_32x32x16_f16 v[18:33], v[134:137], v[86:89], v[18:33]
	ds_read_b128 v[130:133], v162 offset:160
	ds_read_b128 v[134:137], v162 offset:8864
	global_load_dwordx4 v[86:89], v[158:159], off
	v_lshl_add_u64 v[158:159], v[158:159], 0, s[72:73]
	s_waitcnt lgkmcnt(5)
	v_mfma_f32_32x32x16_f16 v[2:17], v[114:117], v[82:85], v[2:17]
	s_waitcnt lgkmcnt(4)
	v_mfma_f32_32x32x16_f16 v[18:33], v[118:121], v[82:85], v[18:33]
	ds_read_b128 v[114:117], v162 offset:192
	ds_read_b128 v[118:121], v162 offset:8896
	global_load_dwordx4 v[82:85], v[158:159], off
	v_lshl_add_u64 v[158:159], v[158:159], 0, s[72:73]
	s_waitcnt lgkmcnt(5)
	v_mfma_f32_32x32x16_f16 v[2:17], v[122:125], v[78:81], v[2:17]
	s_waitcnt lgkmcnt(4)
	v_mfma_f32_32x32x16_f16 v[18:33], v[126:129], v[78:81], v[18:33]
	ds_read_b128 v[122:125], v162 offset:224
	ds_read_b128 v[126:129], v162 offset:8928
	global_load_dwordx4 v[78:81], v[158:159], off
	v_lshl_add_u64 v[158:159], v[158:159], 0, s[72:73]
	s_waitcnt lgkmcnt(5)
	v_mfma_f32_32x32x16_f16 v[2:17], v[130:133], v[74:77], v[2:17]
	s_waitcnt lgkmcnt(4)
	v_mfma_f32_32x32x16_f16 v[18:33], v[134:137], v[74:77], v[18:33]
	global_load_dwordx4 v[74:77], v[158:159], off
	v_lshl_add_u64 v[158:159], v[158:159], 0, s[72:73]
	s_waitcnt lgkmcnt(3)
	v_mfma_f32_32x32x16_f16 v[2:17], v[114:117], v[70:73], v[2:17]
	s_waitcnt lgkmcnt(2)
	v_mfma_f32_32x32x16_f16 v[18:33], v[118:121], v[70:73], v[18:33]
	global_load_dwordx4 v[70:73], v[158:159], off
	v_lshl_add_u64 v[158:159], v[158:159], 0, s[72:73]
	s_waitcnt lgkmcnt(1)
	v_mfma_f32_32x32x16_f16 v[2:17], v[122:125], v[66:69], v[2:17]
	s_waitcnt lgkmcnt(0)
	v_mfma_f32_32x32x16_f16 v[18:33], v[126:129], v[66:69], v[18:33]
	global_load_dwordx4 v[66:69], v[158:159], off
	v_lshl_add_u64 v[158:159], v[158:159], 0, s[72:73]
	s_waitcnt lgkmcnt(0)
	s_barrier
	ds_read_b128 v[114:117], v162 offset:17408
	ds_read_b128 v[118:121], v162 offset:26112
	ds_read_b128 v[122:125], v162 offset:17440
	ds_read_b128 v[126:129], v162 offset:26144
	ds_read_b128 v[130:133], v162 offset:17472
	ds_read_b128 v[134:137], v162 offset:26176
	s_waitcnt lgkmcnt(5)
	v_mfma_f32_32x32x16_f16 v[2:17], v[114:117], v[62:65], v[2:17]
	s_waitcnt lgkmcnt(4)
	v_mfma_f32_32x32x16_f16 v[18:33], v[118:121], v[62:65], v[18:33]
	ds_read_b128 v[114:117], v162 offset:17504
	ds_read_b128 v[118:121], v162 offset:26208
	global_load_dwordx4 v[62:65], v[158:159], off
	v_lshl_add_u64 v[158:159], v[158:159], 0, s[72:73]
	s_waitcnt lgkmcnt(5)
	v_mfma_f32_32x32x16_f16 v[2:17], v[122:125], v[58:61], v[2:17]
	s_waitcnt lgkmcnt(4)
	v_mfma_f32_32x32x16_f16 v[18:33], v[126:129], v[58:61], v[18:33]
	ds_read_b128 v[122:125], v162 offset:17536
	ds_read_b128 v[126:129], v162 offset:26240
	global_load_dwordx4 v[58:61], v[158:159], off
	v_lshl_add_u64 v[158:159], v[158:159], 0, s[72:73]
	s_waitcnt lgkmcnt(5)
	v_mfma_f32_32x32x16_f16 v[2:17], v[130:133], v[54:57], v[2:17]
	s_waitcnt lgkmcnt(4)
	v_mfma_f32_32x32x16_f16 v[18:33], v[134:137], v[54:57], v[18:33]
	ds_read_b128 v[130:133], v162 offset:17568
	ds_read_b128 v[134:137], v162 offset:26272
	global_load_dwordx4 v[54:57], v[158:159], off
	v_lshl_add_u64 v[158:159], v[158:159], 0, s[72:73]
	s_waitcnt lgkmcnt(5)
	v_mfma_f32_32x32x16_f16 v[2:17], v[114:117], v[50:53], v[2:17]
	s_waitcnt lgkmcnt(4)
	v_mfma_f32_32x32x16_f16 v[18:33], v[118:121], v[50:53], v[18:33]
	ds_read_b128 v[114:117], v162 offset:17600
	ds_read_b128 v[118:121], v162 offset:26304
	global_load_dwordx4 v[50:53], v[158:159], off
	v_lshl_add_u64 v[158:159], v[158:159], 0, s[72:73]
	s_waitcnt lgkmcnt(5)
	v_mfma_f32_32x32x16_f16 v[2:17], v[122:125], v[46:49], v[2:17]
	s_waitcnt lgkmcnt(4)
	v_mfma_f32_32x32x16_f16 v[18:33], v[126:129], v[46:49], v[18:33]
	ds_read_b128 v[122:125], v162 offset:17632
	ds_read_b128 v[126:129], v162 offset:26336
	global_load_dwordx4 v[46:49], v[158:159], off
	v_lshl_add_u64 v[158:159], v[158:159], 0, s[72:73]
	s_waitcnt lgkmcnt(5)
	v_mfma_f32_32x32x16_f16 v[2:17], v[130:133], v[42:45], v[2:17]
	s_waitcnt lgkmcnt(4)
	v_mfma_f32_32x32x16_f16 v[18:33], v[134:137], v[42:45], v[18:33]
	global_load_dwordx4 v[42:45], v[158:159], off
	v_lshl_add_u64 v[158:159], v[158:159], 0, s[72:73]
	s_waitcnt lgkmcnt(3)
	v_mfma_f32_32x32x16_f16 v[2:17], v[114:117], v[38:41], v[2:17]
	s_waitcnt lgkmcnt(2)
	v_mfma_f32_32x32x16_f16 v[18:33], v[118:121], v[38:41], v[18:33]
	global_load_dwordx4 v[38:41], v[158:159], off
	v_lshl_add_u64 v[158:159], v[158:159], 0, s[72:73]
	s_waitcnt lgkmcnt(1)
	v_mfma_f32_32x32x16_f16 v[2:17], v[122:125], v[34:37], v[2:17]
	s_waitcnt lgkmcnt(0)
	v_mfma_f32_32x32x16_f16 v[18:33], v[126:129], v[34:37], v[18:33]
	global_load_dwordx4 v[34:37], v[158:159], off
	v_lshl_add_u64 v[158:159], v[158:159], 0, s[72:73]
	s_waitcnt lgkmcnt(0)
	s_barrier
	ds_read_b128 v[114:117], v162 offset:34816
	ds_read_b128 v[118:121], v162 offset:43520
	ds_read_b128 v[122:125], v162 offset:34848
	ds_read_b128 v[126:129], v162 offset:43552
	ds_read_b128 v[130:133], v162 offset:34880
	ds_read_b128 v[134:137], v162 offset:43584
	s_waitcnt vmcnt(23)
	s_waitcnt lgkmcnt(5)
	v_mfma_f32_32x32x16_f16 v[2:17], v[114:117], v[94:97], v[2:17]
	s_waitcnt lgkmcnt(4)
	v_mfma_f32_32x32x16_f16 v[18:33], v[118:121], v[94:97], v[18:33]
	ds_read_b128 v[114:117], v162 offset:34912
	ds_read_b128 v[118:121], v162 offset:43616
	global_load_dwordx4 v[94:97], v[158:159], off
	v_lshl_add_u64 v[158:159], v[158:159], 0, s[72:73]
	s_waitcnt vmcnt(23)
	s_waitcnt lgkmcnt(5)
	v_mfma_f32_32x32x16_f16 v[2:17], v[122:125], v[98:101], v[2:17]
	s_waitcnt lgkmcnt(4)
	v_mfma_f32_32x32x16_f16 v[18:33], v[126:129], v[98:101], v[18:33]
	ds_read_b128 v[122:125], v162 offset:34944
	ds_read_b128 v[126:129], v162 offset:43648
	global_load_dwordx4 v[98:101], v[158:159], off
	v_lshl_add_u64 v[158:159], v[158:159], 0, s[72:73]
	s_waitcnt vmcnt(23)
	s_waitcnt lgkmcnt(5)
	v_mfma_f32_32x32x16_f16 v[2:17], v[130:133], v[102:105], v[2:17]
	s_waitcnt lgkmcnt(4)
	v_mfma_f32_32x32x16_f16 v[18:33], v[134:137], v[102:105], v[18:33]
	ds_read_b128 v[130:133], v162 offset:34976
	ds_read_b128 v[134:137], v162 offset:43680
	global_load_dwordx4 v[102:105], v[158:159], off
	v_lshl_add_u64 v[158:159], v[158:159], 0, s[72:73]
	s_waitcnt vmcnt(23)
	s_waitcnt lgkmcnt(5)
	v_mfma_f32_32x32x16_f16 v[2:17], v[114:117], v[106:109], v[2:17]
	s_waitcnt lgkmcnt(4)
	v_mfma_f32_32x32x16_f16 v[18:33], v[118:121], v[106:109], v[18:33]
	ds_read_b128 v[114:117], v162 offset:35008
	ds_read_b128 v[118:121], v162 offset:43712
	global_load_dwordx4 v[106:109], v[158:159], off
	v_lshl_add_u64 v[158:159], v[158:159], 0, s[72:73]
	s_waitcnt vmcnt(23)
	s_waitcnt lgkmcnt(5)
	v_mfma_f32_32x32x16_f16 v[2:17], v[122:125], v[142:145], v[2:17]
	s_waitcnt lgkmcnt(4)
	v_mfma_f32_32x32x16_f16 v[18:33], v[126:129], v[142:145], v[18:33]
	ds_read_b128 v[122:125], v162 offset:35040
	ds_read_b128 v[126:129], v162 offset:43744
	global_load_dwordx4 v[142:145], v[158:159], off
	v_lshl_add_u64 v[158:159], v[158:159], 0, s[72:73]
	s_waitcnt vmcnt(23)
	s_waitcnt lgkmcnt(5)
	v_mfma_f32_32x32x16_f16 v[2:17], v[130:133], v[146:149], v[2:17]
	s_waitcnt lgkmcnt(4)
	v_mfma_f32_32x32x16_f16 v[18:33], v[134:137], v[146:149], v[18:33]
	global_load_dwordx4 v[146:149], v[158:159], off
	v_lshl_add_u64 v[158:159], v[158:159], 0, s[72:73]
	s_waitcnt vmcnt(23)
	s_waitcnt lgkmcnt(3)
	v_mfma_f32_32x32x16_f16 v[2:17], v[114:117], v[150:153], v[2:17]
	s_waitcnt lgkmcnt(2)
	v_mfma_f32_32x32x16_f16 v[18:33], v[118:121], v[150:153], v[18:33]
	global_load_dwordx4 v[150:153], v[158:159], off
	v_lshl_add_u64 v[158:159], v[158:159], 0, s[72:73]
	s_waitcnt vmcnt(23)
	s_waitcnt lgkmcnt(1)
	v_mfma_f32_32x32x16_f16 v[2:17], v[122:125], v[154:157], v[2:17]
	s_waitcnt lgkmcnt(0)
	v_mfma_f32_32x32x16_f16 v[18:33], v[126:129], v[154:157], v[18:33]
	global_load_dwordx4 v[154:157], v[158:159], off
	v_lshl_add_u64 v[158:159], v[158:159], 0, s[72:73]
	s_waitcnt lgkmcnt(0)
	s_barrier
	ds_read_b128 v[114:117], v162 offset:0
	ds_read_b128 v[118:121], v162 offset:8704
	ds_read_b128 v[122:125], v162 offset:32
	ds_read_b128 v[126:129], v162 offset:8736
	ds_read_b128 v[130:133], v162 offset:64
	ds_read_b128 v[134:137], v162 offset:8768
	s_waitcnt vmcnt(23)
	s_waitcnt lgkmcnt(5)
	v_mfma_f32_32x32x16_f16 v[2:17], v[114:117], v[110:113], v[2:17]
	s_waitcnt lgkmcnt(4)
	v_mfma_f32_32x32x16_f16 v[18:33], v[118:121], v[110:113], v[18:33]
	ds_read_b128 v[114:117], v162 offset:96
	ds_read_b128 v[118:121], v162 offset:8800
	global_load_dwordx4 v[110:113], v[158:159], off
	v_lshl_add_u64 v[158:159], v[158:159], 0, s[72:73]
	s_waitcnt vmcnt(23)
	s_waitcnt lgkmcnt(5)
	v_mfma_f32_32x32x16_f16 v[2:17], v[122:125], v[90:93], v[2:17]
	s_waitcnt lgkmcnt(4)
	v_mfma_f32_32x32x16_f16 v[18:33], v[126:129], v[90:93], v[18:33]
	ds_read_b128 v[122:125], v162 offset:128
	ds_read_b128 v[126:129], v162 offset:8832
	global_load_dwordx4 v[90:93], v[158:159], off
	v_lshl_add_u64 v[158:159], v[158:159], 0, s[72:73]
	s_waitcnt vmcnt(23)
	s_waitcnt lgkmcnt(5)
	v_mfma_f32_32x32x16_f16 v[2:17], v[130:133], v[86:89], v[2:17]
	s_waitcnt lgkmcnt(4)
	v_mfma_f32_32x32x16_f16 v[18:33], v[134:137], v[86:89], v[18:33]
	ds_read_b128 v[130:133], v162 offset:160
	ds_read_b128 v[134:137], v162 offset:8864
	global_load_dwordx4 v[86:89], v[158:159], off
	v_lshl_add_u64 v[158:159], v[158:159], 0, s[72:73]
	s_waitcnt vmcnt(23)
	s_waitcnt lgkmcnt(5)
	v_mfma_f32_32x32x16_f16 v[2:17], v[114:117], v[82:85], v[2:17]
	s_waitcnt lgkmcnt(4)
	v_mfma_f32_32x32x16_f16 v[18:33], v[118:121], v[82:85], v[18:33]
	ds_read_b128 v[114:117], v162 offset:192
	ds_read_b128 v[118:121], v162 offset:8896
	global_load_dwordx4 v[82:85], v[158:159], off
	v_lshl_add_u64 v[158:159], v[158:159], 0, s[72:73]
	s_waitcnt vmcnt(23)
	s_waitcnt lgkmcnt(5)
	v_mfma_f32_32x32x16_f16 v[2:17], v[122:125], v[78:81], v[2:17]
	s_waitcnt lgkmcnt(4)
	v_mfma_f32_32x32x16_f16 v[18:33], v[126:129], v[78:81], v[18:33]
	ds_read_b128 v[122:125], v162 offset:224
	ds_read_b128 v[126:129], v162 offset:8928
	global_load_dwordx4 v[78:81], v[158:159], off
	v_lshl_add_u64 v[158:159], v[158:159], 0, s[72:73]
	s_waitcnt vmcnt(23)
	s_waitcnt lgkmcnt(5)
	v_mfma_f32_32x32x16_f16 v[2:17], v[130:133], v[74:77], v[2:17]
	s_waitcnt lgkmcnt(4)
	v_mfma_f32_32x32x16_f16 v[18:33], v[134:137], v[74:77], v[18:33]
	global_load_dwordx4 v[74:77], v[158:159], off
	v_lshl_add_u64 v[158:159], v[158:159], 0, s[72:73]
	s_waitcnt vmcnt(23)
	s_waitcnt lgkmcnt(3)
	v_mfma_f32_32x32x16_f16 v[2:17], v[114:117], v[70:73], v[2:17]
	s_waitcnt lgkmcnt(2)
	v_mfma_f32_32x32x16_f16 v[18:33], v[118:121], v[70:73], v[18:33]
	global_load_dwordx4 v[70:73], v[158:159], off
	v_lshl_add_u64 v[158:159], v[158:159], 0, s[72:73]
	s_waitcnt vmcnt(23)
	s_waitcnt lgkmcnt(1)
	v_mfma_f32_32x32x16_f16 v[2:17], v[122:125], v[66:69], v[2:17]
	s_waitcnt lgkmcnt(0)
	v_mfma_f32_32x32x16_f16 v[18:33], v[126:129], v[66:69], v[18:33]
	global_load_dwordx4 v[66:69], v[158:159], off
	v_lshl_add_u64 v[158:159], v[158:159], 0, s[72:73]
	s_waitcnt lgkmcnt(0)
	s_barrier
	ds_read_b128 v[114:117], v162 offset:17408
	ds_read_b128 v[118:121], v162 offset:26112
	ds_read_b128 v[122:125], v162 offset:17440
	ds_read_b128 v[126:129], v162 offset:26144
	ds_read_b128 v[130:133], v162 offset:17472
	ds_read_b128 v[134:137], v162 offset:26176
	s_waitcnt vmcnt(23)
	s_waitcnt lgkmcnt(5)
	v_mfma_f32_32x32x16_f16 v[2:17], v[114:117], v[62:65], v[2:17]
	s_waitcnt lgkmcnt(4)
	v_mfma_f32_32x32x16_f16 v[18:33], v[118:121], v[62:65], v[18:33]
	ds_read_b128 v[114:117], v162 offset:17504
	ds_read_b128 v[118:121], v162 offset:26208
	global_load_dwordx4 v[62:65], v[158:159], off
	v_lshl_add_u64 v[158:159], v[158:159], 0, s[72:73]
	s_waitcnt vmcnt(23)
	s_waitcnt lgkmcnt(5)
	v_mfma_f32_32x32x16_f16 v[2:17], v[122:125], v[58:61], v[2:17]
	s_waitcnt lgkmcnt(4)
	v_mfma_f32_32x32x16_f16 v[18:33], v[126:129], v[58:61], v[18:33]
	ds_read_b128 v[122:125], v162 offset:17536
	ds_read_b128 v[126:129], v162 offset:26240
	global_load_dwordx4 v[58:61], v[158:159], off
	v_lshl_add_u64 v[158:159], v[158:159], 0, s[72:73]
	s_waitcnt vmcnt(23)
	s_waitcnt lgkmcnt(5)
	v_mfma_f32_32x32x16_f16 v[2:17], v[130:133], v[54:57], v[2:17]
	s_waitcnt lgkmcnt(4)
	v_mfma_f32_32x32x16_f16 v[18:33], v[134:137], v[54:57], v[18:33]
	ds_read_b128 v[130:133], v162 offset:17568
	ds_read_b128 v[134:137], v162 offset:26272
	global_load_dwordx4 v[54:57], v[158:159], off
	v_lshl_add_u64 v[158:159], v[158:159], 0, s[72:73]
	s_waitcnt vmcnt(23)
	s_waitcnt lgkmcnt(5)
	v_mfma_f32_32x32x16_f16 v[2:17], v[114:117], v[50:53], v[2:17]
	s_waitcnt lgkmcnt(4)
	v_mfma_f32_32x32x16_f16 v[18:33], v[118:121], v[50:53], v[18:33]
	ds_read_b128 v[114:117], v162 offset:17600
	ds_read_b128 v[118:121], v162 offset:26304
	global_load_dwordx4 v[50:53], v[158:159], off
	v_lshl_add_u64 v[158:159], v[158:159], 0, s[72:73]
	s_waitcnt vmcnt(23)
	s_waitcnt lgkmcnt(5)
	v_mfma_f32_32x32x16_f16 v[2:17], v[122:125], v[46:49], v[2:17]
	s_waitcnt lgkmcnt(4)
	v_mfma_f32_32x32x16_f16 v[18:33], v[126:129], v[46:49], v[18:33]
	ds_read_b128 v[122:125], v162 offset:17632
	ds_read_b128 v[126:129], v162 offset:26336
	global_load_dwordx4 v[46:49], v[158:159], off
	v_lshl_add_u64 v[158:159], v[158:159], 0, s[72:73]
	s_waitcnt vmcnt(23)
	s_waitcnt lgkmcnt(5)
	v_mfma_f32_32x32x16_f16 v[2:17], v[130:133], v[42:45], v[2:17]
	s_waitcnt lgkmcnt(4)
	v_mfma_f32_32x32x16_f16 v[18:33], v[134:137], v[42:45], v[18:33]
	global_load_dwordx4 v[42:45], v[158:159], off
	v_lshl_add_u64 v[158:159], v[158:159], 0, s[72:73]
	s_waitcnt vmcnt(23)
	s_waitcnt lgkmcnt(3)
	v_mfma_f32_32x32x16_f16 v[2:17], v[114:117], v[38:41], v[2:17]
	s_waitcnt lgkmcnt(2)
	v_mfma_f32_32x32x16_f16 v[18:33], v[118:121], v[38:41], v[18:33]
	global_load_dwordx4 v[38:41], v[158:159], off
	v_lshl_add_u64 v[158:159], v[158:159], 0, s[72:73]
	s_waitcnt vmcnt(23)
	s_waitcnt lgkmcnt(1)
	v_mfma_f32_32x32x16_f16 v[2:17], v[122:125], v[34:37], v[2:17]
	s_waitcnt lgkmcnt(0)
	v_mfma_f32_32x32x16_f16 v[18:33], v[126:129], v[34:37], v[18:33]
	global_load_dwordx4 v[34:37], v[158:159], off
	v_lshl_add_u64 v[158:159], v[158:159], 0, s[72:73]
	s_waitcnt lgkmcnt(0)
	s_barrier
	ds_read_b128 v[114:117], v162 offset:34816
	ds_read_b128 v[118:121], v162 offset:43520
	ds_read_b128 v[122:125], v162 offset:34848
	ds_read_b128 v[126:129], v162 offset:43552
	ds_read_b128 v[130:133], v162 offset:34880
	ds_read_b128 v[134:137], v162 offset:43584
	s_waitcnt vmcnt(23)
	s_waitcnt lgkmcnt(5)
	v_mfma_f32_32x32x16_f16 v[2:17], v[114:117], v[94:97], v[2:17]
	s_waitcnt lgkmcnt(4)
	v_mfma_f32_32x32x16_f16 v[18:33], v[118:121], v[94:97], v[18:33]
	ds_read_b128 v[114:117], v162 offset:34912
	ds_read_b128 v[118:121], v162 offset:43616
	global_load_dwordx4 v[94:97], v[158:159], off
	v_lshl_add_u64 v[158:159], v[158:159], 0, s[72:73]
	s_waitcnt vmcnt(23)
	s_waitcnt lgkmcnt(5)
	v_mfma_f32_32x32x16_f16 v[2:17], v[122:125], v[98:101], v[2:17]
	s_waitcnt lgkmcnt(4)
	v_mfma_f32_32x32x16_f16 v[18:33], v[126:129], v[98:101], v[18:33]
	ds_read_b128 v[122:125], v162 offset:34944
	ds_read_b128 v[126:129], v162 offset:43648
	global_load_dwordx4 v[98:101], v[158:159], off
	v_lshl_add_u64 v[158:159], v[158:159], 0, s[72:73]
	s_waitcnt vmcnt(23)
	s_waitcnt lgkmcnt(5)
	v_mfma_f32_32x32x16_f16 v[2:17], v[130:133], v[102:105], v[2:17]
	s_waitcnt lgkmcnt(4)
	v_mfma_f32_32x32x16_f16 v[18:33], v[134:137], v[102:105], v[18:33]
	ds_read_b128 v[130:133], v162 offset:34976
	ds_read_b128 v[134:137], v162 offset:43680
	global_load_dwordx4 v[102:105], v[158:159], off
	v_lshl_add_u64 v[158:159], v[158:159], 0, s[72:73]
	s_waitcnt vmcnt(23)
	s_waitcnt lgkmcnt(5)
	v_mfma_f32_32x32x16_f16 v[2:17], v[114:117], v[106:109], v[2:17]
	s_waitcnt lgkmcnt(4)
	v_mfma_f32_32x32x16_f16 v[18:33], v[118:121], v[106:109], v[18:33]
	ds_read_b128 v[114:117], v162 offset:35008
	ds_read_b128 v[118:121], v162 offset:43712
	global_load_dwordx4 v[106:109], v[158:159], off
	v_lshl_add_u64 v[158:159], v[158:159], 0, s[72:73]
	s_waitcnt vmcnt(23)
	s_waitcnt lgkmcnt(5)
	v_mfma_f32_32x32x16_f16 v[2:17], v[122:125], v[142:145], v[2:17]
	s_waitcnt lgkmcnt(4)
	v_mfma_f32_32x32x16_f16 v[18:33], v[126:129], v[142:145], v[18:33]
	ds_read_b128 v[122:125], v162 offset:35040
	ds_read_b128 v[126:129], v162 offset:43744
	global_load_dwordx4 v[142:145], v[158:159], off
	v_lshl_add_u64 v[158:159], v[158:159], 0, s[72:73]
	s_waitcnt vmcnt(23)
	s_waitcnt lgkmcnt(5)
	v_mfma_f32_32x32x16_f16 v[2:17], v[130:133], v[146:149], v[2:17]
	s_waitcnt lgkmcnt(4)
	v_mfma_f32_32x32x16_f16 v[18:33], v[134:137], v[146:149], v[18:33]
	global_load_dwordx4 v[146:149], v[158:159], off
	v_lshl_add_u64 v[158:159], v[158:159], 0, s[72:73]
	s_waitcnt vmcnt(23)
	s_waitcnt lgkmcnt(3)
	v_mfma_f32_32x32x16_f16 v[2:17], v[114:117], v[150:153], v[2:17]
	s_waitcnt lgkmcnt(2)
	v_mfma_f32_32x32x16_f16 v[18:33], v[118:121], v[150:153], v[18:33]
	global_load_dwordx4 v[150:153], v[158:159], off
	v_lshl_add_u64 v[158:159], v[158:159], 0, s[72:73]
	s_waitcnt vmcnt(23)
	s_waitcnt lgkmcnt(1)
	v_mfma_f32_32x32x16_f16 v[2:17], v[122:125], v[154:157], v[2:17]
	s_waitcnt lgkmcnt(0)
	v_mfma_f32_32x32x16_f16 v[18:33], v[126:129], v[154:157], v[18:33]
	global_load_dwordx4 v[154:157], v[158:159], off
	v_lshl_add_u64 v[158:159], v[158:159], 0, s[72:73]
	s_waitcnt lgkmcnt(0)
	s_barrier
	ds_read_b128 v[114:117], v162 offset:0
	ds_read_b128 v[118:121], v162 offset:8704
	ds_read_b128 v[122:125], v162 offset:32
	ds_read_b128 v[126:129], v162 offset:8736
	ds_read_b128 v[130:133], v162 offset:64
	ds_read_b128 v[134:137], v162 offset:8768
	s_waitcnt vmcnt(23)
	s_waitcnt lgkmcnt(5)
	v_mfma_f32_32x32x16_f16 v[2:17], v[114:117], v[110:113], v[2:17]
	s_waitcnt lgkmcnt(4)
	v_mfma_f32_32x32x16_f16 v[18:33], v[118:121], v[110:113], v[18:33]
	ds_read_b128 v[114:117], v162 offset:96
	ds_read_b128 v[118:121], v162 offset:8800
	global_load_dwordx4 v[110:113], v[158:159], off
	v_lshl_add_u64 v[158:159], v[158:159], 0, s[72:73]
	s_waitcnt vmcnt(23)
	s_waitcnt lgkmcnt(5)
	v_mfma_f32_32x32x16_f16 v[2:17], v[122:125], v[90:93], v[2:17]
	s_waitcnt lgkmcnt(4)
	v_mfma_f32_32x32x16_f16 v[18:33], v[126:129], v[90:93], v[18:33]
	ds_read_b128 v[122:125], v162 offset:128
	ds_read_b128 v[126:129], v162 offset:8832
	global_load_dwordx4 v[90:93], v[158:159], off
	v_lshl_add_u64 v[158:159], v[158:159], 0, s[72:73]
	s_waitcnt vmcnt(23)
	s_waitcnt lgkmcnt(5)
	v_mfma_f32_32x32x16_f16 v[2:17], v[130:133], v[86:89], v[2:17]
	s_waitcnt lgkmcnt(4)
	v_mfma_f32_32x32x16_f16 v[18:33], v[134:137], v[86:89], v[18:33]
	ds_read_b128 v[130:133], v162 offset:160
	ds_read_b128 v[134:137], v162 offset:8864
	global_load_dwordx4 v[86:89], v[158:159], off
	v_lshl_add_u64 v[158:159], v[158:159], 0, s[72:73]
	s_waitcnt vmcnt(23)
	s_waitcnt lgkmcnt(5)
	v_mfma_f32_32x32x16_f16 v[2:17], v[114:117], v[82:85], v[2:17]
	s_waitcnt lgkmcnt(4)
	v_mfma_f32_32x32x16_f16 v[18:33], v[118:121], v[82:85], v[18:33]
	ds_read_b128 v[114:117], v162 offset:192
	ds_read_b128 v[118:121], v162 offset:8896
	global_load_dwordx4 v[82:85], v[158:159], off
	v_lshl_add_u64 v[158:159], v[158:159], 0, s[72:73]
	s_waitcnt vmcnt(23)
	s_waitcnt lgkmcnt(5)
	v_mfma_f32_32x32x16_f16 v[2:17], v[122:125], v[78:81], v[2:17]
	s_waitcnt lgkmcnt(4)
	v_mfma_f32_32x32x16_f16 v[18:33], v[126:129], v[78:81], v[18:33]
	ds_read_b128 v[122:125], v162 offset:224
	ds_read_b128 v[126:129], v162 offset:8928
	global_load_dwordx4 v[78:81], v[158:159], off
	v_lshl_add_u64 v[158:159], v[158:159], 0, s[72:73]
	s_waitcnt vmcnt(23)
	s_waitcnt lgkmcnt(5)
	v_mfma_f32_32x32x16_f16 v[2:17], v[130:133], v[74:77], v[2:17]
	s_waitcnt lgkmcnt(4)
	v_mfma_f32_32x32x16_f16 v[18:33], v[134:137], v[74:77], v[18:33]
	global_load_dwordx4 v[74:77], v[158:159], off
	v_lshl_add_u64 v[158:159], v[158:159], 0, s[72:73]
	s_waitcnt vmcnt(23)
	s_waitcnt lgkmcnt(3)
	v_mfma_f32_32x32x16_f16 v[2:17], v[114:117], v[70:73], v[2:17]
	s_waitcnt lgkmcnt(2)
	v_mfma_f32_32x32x16_f16 v[18:33], v[118:121], v[70:73], v[18:33]
	global_load_dwordx4 v[70:73], v[158:159], off
	v_lshl_add_u64 v[158:159], v[158:159], 0, s[72:73]
	s_waitcnt vmcnt(23)
	s_waitcnt lgkmcnt(1)
	v_mfma_f32_32x32x16_f16 v[2:17], v[122:125], v[66:69], v[2:17]
	s_waitcnt lgkmcnt(0)
	v_mfma_f32_32x32x16_f16 v[18:33], v[126:129], v[66:69], v[18:33]
	global_load_dwordx4 v[66:69], v[158:159], off
	v_lshl_add_u64 v[158:159], v[158:159], 0, s[72:73]
	s_waitcnt lgkmcnt(0)
	s_barrier
	ds_read_b128 v[114:117], v162 offset:17408
	ds_read_b128 v[118:121], v162 offset:26112
	ds_read_b128 v[122:125], v162 offset:17440
	ds_read_b128 v[126:129], v162 offset:26144
	ds_read_b128 v[130:133], v162 offset:17472
	ds_read_b128 v[134:137], v162 offset:26176
	s_waitcnt vmcnt(23)
	s_waitcnt lgkmcnt(5)
	v_mfma_f32_32x32x16_f16 v[2:17], v[114:117], v[62:65], v[2:17]
	s_waitcnt lgkmcnt(4)
	v_mfma_f32_32x32x16_f16 v[18:33], v[118:121], v[62:65], v[18:33]
	ds_read_b128 v[114:117], v162 offset:17504
	ds_read_b128 v[118:121], v162 offset:26208
	global_load_dwordx4 v[62:65], v[158:159], off
	v_lshl_add_u64 v[158:159], v[158:159], 0, s[72:73]
	s_waitcnt vmcnt(23)
	s_waitcnt lgkmcnt(5)
	v_mfma_f32_32x32x16_f16 v[2:17], v[122:125], v[58:61], v[2:17]
	s_waitcnt lgkmcnt(4)
	v_mfma_f32_32x32x16_f16 v[18:33], v[126:129], v[58:61], v[18:33]
	ds_read_b128 v[122:125], v162 offset:17536
	ds_read_b128 v[126:129], v162 offset:26240
	global_load_dwordx4 v[58:61], v[158:159], off
	v_lshl_add_u64 v[158:159], v[158:159], 0, s[72:73]
	s_waitcnt vmcnt(23)
	s_waitcnt lgkmcnt(5)
	v_mfma_f32_32x32x16_f16 v[2:17], v[130:133], v[54:57], v[2:17]
	s_waitcnt lgkmcnt(4)
	v_mfma_f32_32x32x16_f16 v[18:33], v[134:137], v[54:57], v[18:33]
	ds_read_b128 v[130:133], v162 offset:17568
	ds_read_b128 v[134:137], v162 offset:26272
	global_load_dwordx4 v[54:57], v[158:159], off
	v_lshl_add_u64 v[158:159], v[158:159], 0, s[72:73]
	s_waitcnt vmcnt(23)
	s_waitcnt lgkmcnt(5)
	v_mfma_f32_32x32x16_f16 v[2:17], v[114:117], v[50:53], v[2:17]
	s_waitcnt lgkmcnt(4)
	v_mfma_f32_32x32x16_f16 v[18:33], v[118:121], v[50:53], v[18:33]
	ds_read_b128 v[114:117], v162 offset:17600
	ds_read_b128 v[118:121], v162 offset:26304
	global_load_dwordx4 v[50:53], v[158:159], off
	v_lshl_add_u64 v[158:159], v[158:159], 0, s[72:73]
	s_waitcnt vmcnt(23)
	s_waitcnt lgkmcnt(5)
	v_mfma_f32_32x32x16_f16 v[2:17], v[122:125], v[46:49], v[2:17]
	s_waitcnt lgkmcnt(4)
	v_mfma_f32_32x32x16_f16 v[18:33], v[126:129], v[46:49], v[18:33]
	ds_read_b128 v[122:125], v162 offset:17632
	ds_read_b128 v[126:129], v162 offset:26336
	global_load_dwordx4 v[46:49], v[158:159], off
	v_lshl_add_u64 v[158:159], v[158:159], 0, s[72:73]
	s_waitcnt vmcnt(23)
	s_waitcnt lgkmcnt(5)
	v_mfma_f32_32x32x16_f16 v[2:17], v[130:133], v[42:45], v[2:17]
	s_waitcnt lgkmcnt(4)
	v_mfma_f32_32x32x16_f16 v[18:33], v[134:137], v[42:45], v[18:33]
	global_load_dwordx4 v[42:45], v[158:159], off
	v_lshl_add_u64 v[158:159], v[158:159], 0, s[72:73]
	s_waitcnt vmcnt(23)
	s_waitcnt lgkmcnt(3)
	v_mfma_f32_32x32x16_f16 v[2:17], v[114:117], v[38:41], v[2:17]
	s_waitcnt lgkmcnt(2)
	v_mfma_f32_32x32x16_f16 v[18:33], v[118:121], v[38:41], v[18:33]
	global_load_dwordx4 v[38:41], v[158:159], off
	v_lshl_add_u64 v[158:159], v[158:159], 0, s[72:73]
	s_waitcnt vmcnt(23)
	s_waitcnt lgkmcnt(1)
	v_mfma_f32_32x32x16_f16 v[2:17], v[122:125], v[34:37], v[2:17]
	s_waitcnt lgkmcnt(0)
	v_mfma_f32_32x32x16_f16 v[18:33], v[126:129], v[34:37], v[18:33]
	global_load_dwordx4 v[34:37], v[158:159], off
	v_lshl_add_u64 v[158:159], v[158:159], 0, s[72:73]
	s_waitcnt lgkmcnt(0)
	s_barrier
	ds_read_b128 v[114:117], v162 offset:34816
	ds_read_b128 v[118:121], v162 offset:43520
	ds_read_b128 v[122:125], v162 offset:34848
	ds_read_b128 v[126:129], v162 offset:43552
	ds_read_b128 v[130:133], v162 offset:34880
	ds_read_b128 v[134:137], v162 offset:43584
	s_waitcnt vmcnt(23)
	s_waitcnt lgkmcnt(5)
	v_mfma_f32_32x32x16_f16 v[2:17], v[114:117], v[94:97], v[2:17]
	s_waitcnt lgkmcnt(4)
	v_mfma_f32_32x32x16_f16 v[18:33], v[118:121], v[94:97], v[18:33]
	ds_read_b128 v[114:117], v162 offset:34912
	ds_read_b128 v[118:121], v162 offset:43616
	global_load_dwordx4 v[94:97], v[158:159], off
	v_lshl_add_u64 v[158:159], v[158:159], 0, s[72:73]
	s_waitcnt vmcnt(23)
	s_waitcnt lgkmcnt(5)
	v_mfma_f32_32x32x16_f16 v[2:17], v[122:125], v[98:101], v[2:17]
	s_waitcnt lgkmcnt(4)
	v_mfma_f32_32x32x16_f16 v[18:33], v[126:129], v[98:101], v[18:33]
	ds_read_b128 v[122:125], v162 offset:34944
	ds_read_b128 v[126:129], v162 offset:43648
	global_load_dwordx4 v[98:101], v[158:159], off
	v_lshl_add_u64 v[158:159], v[158:159], 0, s[72:73]
	s_waitcnt vmcnt(23)
	s_waitcnt lgkmcnt(5)
	v_mfma_f32_32x32x16_f16 v[2:17], v[130:133], v[102:105], v[2:17]
	s_waitcnt lgkmcnt(4)
	v_mfma_f32_32x32x16_f16 v[18:33], v[134:137], v[102:105], v[18:33]
	ds_read_b128 v[130:133], v162 offset:34976
	ds_read_b128 v[134:137], v162 offset:43680
	global_load_dwordx4 v[102:105], v[158:159], off
	v_lshl_add_u64 v[158:159], v[158:159], 0, s[72:73]
	s_waitcnt vmcnt(23)
	s_waitcnt lgkmcnt(5)
	v_mfma_f32_32x32x16_f16 v[2:17], v[114:117], v[106:109], v[2:17]
	s_waitcnt lgkmcnt(4)
	v_mfma_f32_32x32x16_f16 v[18:33], v[118:121], v[106:109], v[18:33]
	ds_read_b128 v[114:117], v162 offset:35008
	ds_read_b128 v[118:121], v162 offset:43712
	global_load_dwordx4 v[106:109], v[158:159], off
	v_lshl_add_u64 v[158:159], v[158:159], 0, s[72:73]
	s_waitcnt vmcnt(23)
	s_waitcnt lgkmcnt(5)
	v_mfma_f32_32x32x16_f16 v[2:17], v[122:125], v[142:145], v[2:17]
	s_waitcnt lgkmcnt(4)
	v_mfma_f32_32x32x16_f16 v[18:33], v[126:129], v[142:145], v[18:33]
	ds_read_b128 v[122:125], v162 offset:35040
	ds_read_b128 v[126:129], v162 offset:43744
	global_load_dwordx4 v[142:145], v[158:159], off
	v_lshl_add_u64 v[158:159], v[158:159], 0, s[72:73]
	s_waitcnt vmcnt(23)
	s_waitcnt lgkmcnt(5)
	v_mfma_f32_32x32x16_f16 v[2:17], v[130:133], v[146:149], v[2:17]
	s_waitcnt lgkmcnt(4)
	v_mfma_f32_32x32x16_f16 v[18:33], v[134:137], v[146:149], v[18:33]
	global_load_dwordx4 v[146:149], v[158:159], off
	v_lshl_add_u64 v[158:159], v[158:159], 0, s[72:73]
	s_waitcnt vmcnt(23)
	s_waitcnt lgkmcnt(3)
	v_mfma_f32_32x32x16_f16 v[2:17], v[114:117], v[150:153], v[2:17]
	s_waitcnt lgkmcnt(2)
	v_mfma_f32_32x32x16_f16 v[18:33], v[118:121], v[150:153], v[18:33]
	global_load_dwordx4 v[150:153], v[158:159], off
	v_lshl_add_u64 v[158:159], v[158:159], 0, s[72:73]
	s_waitcnt vmcnt(23)
	s_waitcnt lgkmcnt(1)
	v_mfma_f32_32x32x16_f16 v[2:17], v[122:125], v[154:157], v[2:17]
	s_waitcnt lgkmcnt(0)
	v_mfma_f32_32x32x16_f16 v[18:33], v[126:129], v[154:157], v[18:33]
	global_load_dwordx4 v[154:157], v[158:159], off
	v_lshl_add_u64 v[158:159], v[158:159], 0, s[72:73]
	s_waitcnt lgkmcnt(0)
	s_barrier
	ds_read_b128 v[114:117], v162 offset:0
	ds_read_b128 v[118:121], v162 offset:8704
	ds_read_b128 v[122:125], v162 offset:32
	ds_read_b128 v[126:129], v162 offset:8736
	ds_read_b128 v[130:133], v162 offset:64
	ds_read_b128 v[134:137], v162 offset:8768
	s_waitcnt vmcnt(23)
	s_waitcnt lgkmcnt(5)
	v_mfma_f32_32x32x16_f16 v[2:17], v[114:117], v[110:113], v[2:17]
	s_waitcnt lgkmcnt(4)
	v_mfma_f32_32x32x16_f16 v[18:33], v[118:121], v[110:113], v[18:33]
	ds_read_b128 v[114:117], v162 offset:96
	ds_read_b128 v[118:121], v162 offset:8800
	global_load_dwordx4 v[110:113], v[158:159], off
	v_lshl_add_u64 v[158:159], v[158:159], 0, s[72:73]
	s_waitcnt vmcnt(23)
	s_waitcnt lgkmcnt(5)
	v_mfma_f32_32x32x16_f16 v[2:17], v[122:125], v[90:93], v[2:17]
	s_waitcnt lgkmcnt(4)
	v_mfma_f32_32x32x16_f16 v[18:33], v[126:129], v[90:93], v[18:33]
	ds_read_b128 v[122:125], v162 offset:128
	ds_read_b128 v[126:129], v162 offset:8832
	global_load_dwordx4 v[90:93], v[158:159], off
	v_lshl_add_u64 v[158:159], v[158:159], 0, s[72:73]
	s_waitcnt vmcnt(23)
	s_waitcnt lgkmcnt(5)
	v_mfma_f32_32x32x16_f16 v[2:17], v[130:133], v[86:89], v[2:17]
	s_waitcnt lgkmcnt(4)
	v_mfma_f32_32x32x16_f16 v[18:33], v[134:137], v[86:89], v[18:33]
	ds_read_b128 v[130:133], v162 offset:160
	ds_read_b128 v[134:137], v162 offset:8864
	global_load_dwordx4 v[86:89], v[158:159], off
	v_lshl_add_u64 v[158:159], v[158:159], 0, s[72:73]
	s_waitcnt vmcnt(23)
	s_waitcnt lgkmcnt(5)
	v_mfma_f32_32x32x16_f16 v[2:17], v[114:117], v[82:85], v[2:17]
	s_waitcnt lgkmcnt(4)
	v_mfma_f32_32x32x16_f16 v[18:33], v[118:121], v[82:85], v[18:33]
	ds_read_b128 v[114:117], v162 offset:192
	ds_read_b128 v[118:121], v162 offset:8896
	global_load_dwordx4 v[82:85], v[158:159], off
	v_lshl_add_u64 v[158:159], v[158:159], 0, s[72:73]
	s_waitcnt vmcnt(23)
	s_waitcnt lgkmcnt(5)
	v_mfma_f32_32x32x16_f16 v[2:17], v[122:125], v[78:81], v[2:17]
	s_waitcnt lgkmcnt(4)
	v_mfma_f32_32x32x16_f16 v[18:33], v[126:129], v[78:81], v[18:33]
	ds_read_b128 v[122:125], v162 offset:224
	ds_read_b128 v[126:129], v162 offset:8928
	global_load_dwordx4 v[78:81], v[158:159], off
	v_lshl_add_u64 v[158:159], v[158:159], 0, s[72:73]
	s_waitcnt vmcnt(23)
	s_waitcnt lgkmcnt(5)
	v_mfma_f32_32x32x16_f16 v[2:17], v[130:133], v[74:77], v[2:17]
	s_waitcnt lgkmcnt(4)
	v_mfma_f32_32x32x16_f16 v[18:33], v[134:137], v[74:77], v[18:33]
	global_load_dwordx4 v[74:77], v[158:159], off
	v_lshl_add_u64 v[158:159], v[158:159], 0, s[72:73]
	s_waitcnt vmcnt(23)
	s_waitcnt lgkmcnt(3)
	v_mfma_f32_32x32x16_f16 v[2:17], v[114:117], v[70:73], v[2:17]
	s_waitcnt lgkmcnt(2)
	v_mfma_f32_32x32x16_f16 v[18:33], v[118:121], v[70:73], v[18:33]
	global_load_dwordx4 v[70:73], v[158:159], off
	v_lshl_add_u64 v[158:159], v[158:159], 0, s[72:73]
	s_waitcnt vmcnt(23)
	s_waitcnt lgkmcnt(1)
	v_mfma_f32_32x32x16_f16 v[2:17], v[122:125], v[66:69], v[2:17]
	s_waitcnt lgkmcnt(0)
	v_mfma_f32_32x32x16_f16 v[18:33], v[126:129], v[66:69], v[18:33]
	global_load_dwordx4 v[66:69], v[158:159], off
	v_lshl_add_u64 v[158:159], v[158:159], 0, s[72:73]
	s_waitcnt lgkmcnt(0)
	s_barrier
	ds_read_b128 v[114:117], v162 offset:17408
	ds_read_b128 v[118:121], v162 offset:26112
	ds_read_b128 v[122:125], v162 offset:17440
	ds_read_b128 v[126:129], v162 offset:26144
	ds_read_b128 v[130:133], v162 offset:17472
	ds_read_b128 v[134:137], v162 offset:26176
	s_waitcnt vmcnt(23)
	s_waitcnt lgkmcnt(5)
	v_mfma_f32_32x32x16_f16 v[2:17], v[114:117], v[62:65], v[2:17]
	s_waitcnt lgkmcnt(4)
	v_mfma_f32_32x32x16_f16 v[18:33], v[118:121], v[62:65], v[18:33]
	ds_read_b128 v[114:117], v162 offset:17504
	ds_read_b128 v[118:121], v162 offset:26208
	global_load_dwordx4 v[62:65], v[158:159], off
	v_lshl_add_u64 v[158:159], v[158:159], 0, s[72:73]
	s_waitcnt vmcnt(23)
	s_waitcnt lgkmcnt(5)
	v_mfma_f32_32x32x16_f16 v[2:17], v[122:125], v[58:61], v[2:17]
	s_waitcnt lgkmcnt(4)
	v_mfma_f32_32x32x16_f16 v[18:33], v[126:129], v[58:61], v[18:33]
	ds_read_b128 v[122:125], v162 offset:17536
	ds_read_b128 v[126:129], v162 offset:26240
	global_load_dwordx4 v[58:61], v[158:159], off
	v_lshl_add_u64 v[158:159], v[158:159], 0, s[72:73]
	s_waitcnt vmcnt(23)
	s_waitcnt lgkmcnt(5)
	v_mfma_f32_32x32x16_f16 v[2:17], v[130:133], v[54:57], v[2:17]
	s_waitcnt lgkmcnt(4)
	v_mfma_f32_32x32x16_f16 v[18:33], v[134:137], v[54:57], v[18:33]
	ds_read_b128 v[130:133], v162 offset:17568
	ds_read_b128 v[134:137], v162 offset:26272
	global_load_dwordx4 v[54:57], v[158:159], off
	v_lshl_add_u64 v[158:159], v[158:159], 0, s[72:73]
	s_waitcnt vmcnt(23)
	s_waitcnt lgkmcnt(5)
	v_mfma_f32_32x32x16_f16 v[2:17], v[114:117], v[50:53], v[2:17]
	s_waitcnt lgkmcnt(4)
	v_mfma_f32_32x32x16_f16 v[18:33], v[118:121], v[50:53], v[18:33]
	ds_read_b128 v[114:117], v162 offset:17600
	ds_read_b128 v[118:121], v162 offset:26304
	global_load_dwordx4 v[50:53], v[158:159], off
	v_lshl_add_u64 v[158:159], v[158:159], 0, s[72:73]
	s_waitcnt vmcnt(23)
	s_waitcnt lgkmcnt(5)
	v_mfma_f32_32x32x16_f16 v[2:17], v[122:125], v[46:49], v[2:17]
	s_waitcnt lgkmcnt(4)
	v_mfma_f32_32x32x16_f16 v[18:33], v[126:129], v[46:49], v[18:33]
	ds_read_b128 v[122:125], v162 offset:17632
	ds_read_b128 v[126:129], v162 offset:26336
	global_load_dwordx4 v[46:49], v[158:159], off
	v_lshl_add_u64 v[158:159], v[158:159], 0, s[72:73]
	s_waitcnt vmcnt(23)
	s_waitcnt lgkmcnt(5)
	v_mfma_f32_32x32x16_f16 v[2:17], v[130:133], v[42:45], v[2:17]
	s_waitcnt lgkmcnt(4)
	v_mfma_f32_32x32x16_f16 v[18:33], v[134:137], v[42:45], v[18:33]
	global_load_dwordx4 v[42:45], v[158:159], off
	v_lshl_add_u64 v[158:159], v[158:159], 0, s[72:73]
	s_waitcnt vmcnt(23)
	s_waitcnt lgkmcnt(3)
	v_mfma_f32_32x32x16_f16 v[2:17], v[114:117], v[38:41], v[2:17]
	s_waitcnt lgkmcnt(2)
	v_mfma_f32_32x32x16_f16 v[18:33], v[118:121], v[38:41], v[18:33]
	global_load_dwordx4 v[38:41], v[158:159], off
	v_lshl_add_u64 v[158:159], v[158:159], 0, s[72:73]
	s_waitcnt vmcnt(23)
	s_waitcnt lgkmcnt(1)
	v_mfma_f32_32x32x16_f16 v[2:17], v[122:125], v[34:37], v[2:17]
	s_waitcnt lgkmcnt(0)
	v_mfma_f32_32x32x16_f16 v[18:33], v[126:129], v[34:37], v[18:33]
	global_load_dwordx4 v[34:37], v[158:159], off
	v_lshl_add_u64 v[158:159], v[158:159], 0, s[72:73]
	s_waitcnt lgkmcnt(0)
	s_barrier
	ds_read_b128 v[114:117], v162 offset:34816
	ds_read_b128 v[118:121], v162 offset:43520
	ds_read_b128 v[122:125], v162 offset:34848
	ds_read_b128 v[126:129], v162 offset:43552
	ds_read_b128 v[130:133], v162 offset:34880
	ds_read_b128 v[134:137], v162 offset:43584
	s_waitcnt vmcnt(23)
	s_waitcnt lgkmcnt(5)
	v_mfma_f32_32x32x16_f16 v[2:17], v[114:117], v[94:97], v[2:17]
	s_waitcnt lgkmcnt(4)
	v_mfma_f32_32x32x16_f16 v[18:33], v[118:121], v[94:97], v[18:33]
	ds_read_b128 v[114:117], v162 offset:34912
	ds_read_b128 v[118:121], v162 offset:43616
	global_load_dwordx4 v[94:97], v[158:159], off
	v_lshl_add_u64 v[158:159], v[158:159], 0, s[72:73]
	s_waitcnt vmcnt(23)
	s_waitcnt lgkmcnt(5)
	v_mfma_f32_32x32x16_f16 v[2:17], v[122:125], v[98:101], v[2:17]
	s_waitcnt lgkmcnt(4)
	v_mfma_f32_32x32x16_f16 v[18:33], v[126:129], v[98:101], v[18:33]
	ds_read_b128 v[122:125], v162 offset:34944
	ds_read_b128 v[126:129], v162 offset:43648
	global_load_dwordx4 v[98:101], v[158:159], off
	v_lshl_add_u64 v[158:159], v[158:159], 0, s[72:73]
	s_waitcnt vmcnt(23)
	s_waitcnt lgkmcnt(5)
	v_mfma_f32_32x32x16_f16 v[2:17], v[130:133], v[102:105], v[2:17]
	s_waitcnt lgkmcnt(4)
	v_mfma_f32_32x32x16_f16 v[18:33], v[134:137], v[102:105], v[18:33]
	ds_read_b128 v[130:133], v162 offset:34976
	ds_read_b128 v[134:137], v162 offset:43680
	global_load_dwordx4 v[102:105], v[158:159], off
	v_lshl_add_u64 v[158:159], v[158:159], 0, s[72:73]
	s_waitcnt vmcnt(23)
	s_waitcnt lgkmcnt(5)
	v_mfma_f32_32x32x16_f16 v[2:17], v[114:117], v[106:109], v[2:17]
	s_waitcnt lgkmcnt(4)
	v_mfma_f32_32x32x16_f16 v[18:33], v[118:121], v[106:109], v[18:33]
	ds_read_b128 v[114:117], v162 offset:35008
	ds_read_b128 v[118:121], v162 offset:43712
	global_load_dwordx4 v[106:109], v[158:159], off
	v_lshl_add_u64 v[158:159], v[158:159], 0, s[72:73]
	s_waitcnt vmcnt(23)
	s_waitcnt lgkmcnt(5)
	v_mfma_f32_32x32x16_f16 v[2:17], v[122:125], v[142:145], v[2:17]
	s_waitcnt lgkmcnt(4)
	v_mfma_f32_32x32x16_f16 v[18:33], v[126:129], v[142:145], v[18:33]
	ds_read_b128 v[122:125], v162 offset:35040
	ds_read_b128 v[126:129], v162 offset:43744
	global_load_dwordx4 v[142:145], v[158:159], off
	v_lshl_add_u64 v[158:159], v[158:159], 0, s[72:73]
	s_waitcnt vmcnt(23)
	s_waitcnt lgkmcnt(5)
	v_mfma_f32_32x32x16_f16 v[2:17], v[130:133], v[146:149], v[2:17]
	s_waitcnt lgkmcnt(4)
	v_mfma_f32_32x32x16_f16 v[18:33], v[134:137], v[146:149], v[18:33]
	global_load_dwordx4 v[146:149], v[158:159], off
	v_lshl_add_u64 v[158:159], v[158:159], 0, s[72:73]
	s_waitcnt vmcnt(23)
	s_waitcnt lgkmcnt(3)
	v_mfma_f32_32x32x16_f16 v[2:17], v[114:117], v[150:153], v[2:17]
	s_waitcnt lgkmcnt(2)
	v_mfma_f32_32x32x16_f16 v[18:33], v[118:121], v[150:153], v[18:33]
	global_load_dwordx4 v[150:153], v[158:159], off
	v_lshl_add_u64 v[158:159], v[158:159], 0, s[72:73]
	s_waitcnt vmcnt(23)
	s_waitcnt lgkmcnt(1)
	v_mfma_f32_32x32x16_f16 v[2:17], v[122:125], v[154:157], v[2:17]
	s_waitcnt lgkmcnt(0)
	v_mfma_f32_32x32x16_f16 v[18:33], v[126:129], v[154:157], v[18:33]
	global_load_dwordx4 v[154:157], v[158:159], off
	v_lshl_add_u64 v[158:159], v[158:159], 0, s[72:73]
	s_waitcnt lgkmcnt(0)
	s_barrier
	ds_read_b128 v[114:117], v162 offset:0
	ds_read_b128 v[118:121], v162 offset:8704
	ds_read_b128 v[122:125], v162 offset:32
	ds_read_b128 v[126:129], v162 offset:8736
	ds_read_b128 v[130:133], v162 offset:64
	ds_read_b128 v[134:137], v162 offset:8768
	s_waitcnt vmcnt(23)
	s_waitcnt lgkmcnt(5)
	v_mfma_f32_32x32x16_f16 v[2:17], v[114:117], v[110:113], v[2:17]
	s_waitcnt lgkmcnt(4)
	v_mfma_f32_32x32x16_f16 v[18:33], v[118:121], v[110:113], v[18:33]
	ds_read_b128 v[114:117], v162 offset:96
	ds_read_b128 v[118:121], v162 offset:8800
	global_load_dwordx4 v[110:113], v[158:159], off
	v_lshl_add_u64 v[158:159], v[158:159], 0, s[72:73]
	s_waitcnt vmcnt(23)
	s_waitcnt lgkmcnt(5)
	v_mfma_f32_32x32x16_f16 v[2:17], v[122:125], v[90:93], v[2:17]
	s_waitcnt lgkmcnt(4)
	v_mfma_f32_32x32x16_f16 v[18:33], v[126:129], v[90:93], v[18:33]
	ds_read_b128 v[122:125], v162 offset:128
	ds_read_b128 v[126:129], v162 offset:8832
	global_load_dwordx4 v[90:93], v[158:159], off
	v_lshl_add_u64 v[158:159], v[158:159], 0, s[72:73]
	s_waitcnt vmcnt(23)
	s_waitcnt lgkmcnt(5)
	v_mfma_f32_32x32x16_f16 v[2:17], v[130:133], v[86:89], v[2:17]
	s_waitcnt lgkmcnt(4)
	v_mfma_f32_32x32x16_f16 v[18:33], v[134:137], v[86:89], v[18:33]
	ds_read_b128 v[130:133], v162 offset:160
	ds_read_b128 v[134:137], v162 offset:8864
	global_load_dwordx4 v[86:89], v[158:159], off
	v_lshl_add_u64 v[158:159], v[158:159], 0, s[72:73]
	s_waitcnt vmcnt(23)
	s_waitcnt lgkmcnt(5)
	v_mfma_f32_32x32x16_f16 v[2:17], v[114:117], v[82:85], v[2:17]
	s_waitcnt lgkmcnt(4)
	v_mfma_f32_32x32x16_f16 v[18:33], v[118:121], v[82:85], v[18:33]
	ds_read_b128 v[114:117], v162 offset:192
	ds_read_b128 v[118:121], v162 offset:8896
	global_load_dwordx4 v[82:85], v[158:159], off
	v_lshl_add_u64 v[158:159], v[158:159], 0, s[72:73]
	s_waitcnt vmcnt(23)
	s_waitcnt lgkmcnt(5)
	v_mfma_f32_32x32x16_f16 v[2:17], v[122:125], v[78:81], v[2:17]
	s_waitcnt lgkmcnt(4)
	v_mfma_f32_32x32x16_f16 v[18:33], v[126:129], v[78:81], v[18:33]
	ds_read_b128 v[122:125], v162 offset:224
	ds_read_b128 v[126:129], v162 offset:8928
	global_load_dwordx4 v[78:81], v[158:159], off
	v_lshl_add_u64 v[158:159], v[158:159], 0, s[72:73]
	s_waitcnt vmcnt(23)
	s_waitcnt lgkmcnt(5)
	v_mfma_f32_32x32x16_f16 v[2:17], v[130:133], v[74:77], v[2:17]
	s_waitcnt lgkmcnt(4)
	v_mfma_f32_32x32x16_f16 v[18:33], v[134:137], v[74:77], v[18:33]
	global_load_dwordx4 v[74:77], v[158:159], off
	v_lshl_add_u64 v[158:159], v[158:159], 0, s[72:73]
	s_waitcnt vmcnt(23)
	s_waitcnt lgkmcnt(3)
	v_mfma_f32_32x32x16_f16 v[2:17], v[114:117], v[70:73], v[2:17]
	s_waitcnt lgkmcnt(2)
	v_mfma_f32_32x32x16_f16 v[18:33], v[118:121], v[70:73], v[18:33]
	global_load_dwordx4 v[70:73], v[158:159], off
	v_lshl_add_u64 v[158:159], v[158:159], 0, s[72:73]
	s_waitcnt vmcnt(23)
	s_waitcnt lgkmcnt(1)
	v_mfma_f32_32x32x16_f16 v[2:17], v[122:125], v[66:69], v[2:17]
	s_waitcnt lgkmcnt(0)
	v_mfma_f32_32x32x16_f16 v[18:33], v[126:129], v[66:69], v[18:33]
	global_load_dwordx4 v[66:69], v[158:159], off
	v_lshl_add_u64 v[158:159], v[158:159], 0, s[72:73]
	s_waitcnt lgkmcnt(0)
	s_barrier
	ds_read_b128 v[114:117], v162 offset:17408
	ds_read_b128 v[118:121], v162 offset:26112
	ds_read_b128 v[122:125], v162 offset:17440
	ds_read_b128 v[126:129], v162 offset:26144
	ds_read_b128 v[130:133], v162 offset:17472
	ds_read_b128 v[134:137], v162 offset:26176
	s_waitcnt vmcnt(23)
	s_waitcnt lgkmcnt(5)
	v_mfma_f32_32x32x16_f16 v[2:17], v[114:117], v[62:65], v[2:17]
	s_waitcnt lgkmcnt(4)
	v_mfma_f32_32x32x16_f16 v[18:33], v[118:121], v[62:65], v[18:33]
	ds_read_b128 v[114:117], v162 offset:17504
	ds_read_b128 v[118:121], v162 offset:26208
	global_load_dwordx4 v[62:65], v[158:159], off
	v_lshl_add_u64 v[158:159], v[158:159], 0, s[72:73]
	s_waitcnt vmcnt(23)
	s_waitcnt lgkmcnt(5)
	v_mfma_f32_32x32x16_f16 v[2:17], v[122:125], v[58:61], v[2:17]
	s_waitcnt lgkmcnt(4)
	v_mfma_f32_32x32x16_f16 v[18:33], v[126:129], v[58:61], v[18:33]
	ds_read_b128 v[122:125], v162 offset:17536
	ds_read_b128 v[126:129], v162 offset:26240
	global_load_dwordx4 v[58:61], v[158:159], off
	v_lshl_add_u64 v[158:159], v[158:159], 0, s[72:73]
	s_waitcnt vmcnt(23)
	s_waitcnt lgkmcnt(5)
	v_mfma_f32_32x32x16_f16 v[2:17], v[130:133], v[54:57], v[2:17]
	s_waitcnt lgkmcnt(4)
	v_mfma_f32_32x32x16_f16 v[18:33], v[134:137], v[54:57], v[18:33]
	ds_read_b128 v[130:133], v162 offset:17568
	ds_read_b128 v[134:137], v162 offset:26272
	global_load_dwordx4 v[54:57], v[158:159], off
	v_lshl_add_u64 v[158:159], v[158:159], 0, s[72:73]
	s_waitcnt vmcnt(23)
	s_waitcnt lgkmcnt(5)
	v_mfma_f32_32x32x16_f16 v[2:17], v[114:117], v[50:53], v[2:17]
	s_waitcnt lgkmcnt(4)
	v_mfma_f32_32x32x16_f16 v[18:33], v[118:121], v[50:53], v[18:33]
	ds_read_b128 v[114:117], v162 offset:17600
	ds_read_b128 v[118:121], v162 offset:26304
	global_load_dwordx4 v[50:53], v[158:159], off
	v_lshl_add_u64 v[158:159], v[158:159], 0, s[72:73]
	s_waitcnt vmcnt(23)
	s_waitcnt lgkmcnt(5)
	v_mfma_f32_32x32x16_f16 v[2:17], v[122:125], v[46:49], v[2:17]
	s_waitcnt lgkmcnt(4)
	v_mfma_f32_32x32x16_f16 v[18:33], v[126:129], v[46:49], v[18:33]
	ds_read_b128 v[122:125], v162 offset:17632
	ds_read_b128 v[126:129], v162 offset:26336
	global_load_dwordx4 v[46:49], v[158:159], off
	v_lshl_add_u64 v[158:159], v[158:159], 0, s[72:73]
	s_waitcnt vmcnt(23)
	s_waitcnt lgkmcnt(5)
	v_mfma_f32_32x32x16_f16 v[2:17], v[130:133], v[42:45], v[2:17]
	s_waitcnt lgkmcnt(4)
	v_mfma_f32_32x32x16_f16 v[18:33], v[134:137], v[42:45], v[18:33]
	global_load_dwordx4 v[42:45], v[158:159], off
	v_lshl_add_u64 v[158:159], v[158:159], 0, s[72:73]
	s_waitcnt vmcnt(23)
	s_waitcnt lgkmcnt(3)
	v_mfma_f32_32x32x16_f16 v[2:17], v[114:117], v[38:41], v[2:17]
	s_waitcnt lgkmcnt(2)
	v_mfma_f32_32x32x16_f16 v[18:33], v[118:121], v[38:41], v[18:33]
	global_load_dwordx4 v[38:41], v[158:159], off
	v_lshl_add_u64 v[158:159], v[158:159], 0, s[72:73]
	s_waitcnt vmcnt(23)
	s_waitcnt lgkmcnt(1)
	v_mfma_f32_32x32x16_f16 v[2:17], v[122:125], v[34:37], v[2:17]
	s_waitcnt lgkmcnt(0)
	v_mfma_f32_32x32x16_f16 v[18:33], v[126:129], v[34:37], v[18:33]
	global_load_dwordx4 v[34:37], v[158:159], off
	v_lshl_add_u64 v[158:159], v[158:159], 0, s[72:73]
	s_waitcnt lgkmcnt(0)
	s_barrier
	ds_read_b128 v[114:117], v162 offset:34816
	ds_read_b128 v[118:121], v162 offset:43520
	ds_read_b128 v[122:125], v162 offset:34848
	ds_read_b128 v[126:129], v162 offset:43552
	ds_read_b128 v[130:133], v162 offset:34880
	ds_read_b128 v[134:137], v162 offset:43584
	s_waitcnt vmcnt(23)
	s_waitcnt lgkmcnt(5)
	v_mfma_f32_32x32x16_f16 v[2:17], v[114:117], v[94:97], v[2:17]
	s_waitcnt lgkmcnt(4)
	v_mfma_f32_32x32x16_f16 v[18:33], v[118:121], v[94:97], v[18:33]
	ds_read_b128 v[114:117], v162 offset:34912
	ds_read_b128 v[118:121], v162 offset:43616
	global_load_dwordx4 v[94:97], v[158:159], off
	v_lshl_add_u64 v[158:159], v[158:159], 0, s[72:73]
	s_waitcnt vmcnt(23)
	s_waitcnt lgkmcnt(5)
	v_mfma_f32_32x32x16_f16 v[2:17], v[122:125], v[98:101], v[2:17]
	s_waitcnt lgkmcnt(4)
	v_mfma_f32_32x32x16_f16 v[18:33], v[126:129], v[98:101], v[18:33]
	ds_read_b128 v[122:125], v162 offset:34944
	ds_read_b128 v[126:129], v162 offset:43648
	global_load_dwordx4 v[98:101], v[158:159], off
	v_lshl_add_u64 v[158:159], v[158:159], 0, s[72:73]
	s_waitcnt vmcnt(23)
	s_waitcnt lgkmcnt(5)
	v_mfma_f32_32x32x16_f16 v[2:17], v[130:133], v[102:105], v[2:17]
	s_waitcnt lgkmcnt(4)
	v_mfma_f32_32x32x16_f16 v[18:33], v[134:137], v[102:105], v[18:33]
	ds_read_b128 v[130:133], v162 offset:34976
	ds_read_b128 v[134:137], v162 offset:43680
	global_load_dwordx4 v[102:105], v[158:159], off
	v_lshl_add_u64 v[158:159], v[158:159], 0, s[72:73]
	s_waitcnt vmcnt(23)
	s_waitcnt lgkmcnt(5)
	v_mfma_f32_32x32x16_f16 v[2:17], v[114:117], v[106:109], v[2:17]
	s_waitcnt lgkmcnt(4)
	v_mfma_f32_32x32x16_f16 v[18:33], v[118:121], v[106:109], v[18:33]
	ds_read_b128 v[114:117], v162 offset:35008
	ds_read_b128 v[118:121], v162 offset:43712
	global_load_dwordx4 v[106:109], v[158:159], off
	v_lshl_add_u64 v[158:159], v[158:159], 0, s[72:73]
	s_waitcnt vmcnt(23)
	s_waitcnt lgkmcnt(5)
	v_mfma_f32_32x32x16_f16 v[2:17], v[122:125], v[142:145], v[2:17]
	s_waitcnt lgkmcnt(4)
	v_mfma_f32_32x32x16_f16 v[18:33], v[126:129], v[142:145], v[18:33]
	ds_read_b128 v[122:125], v162 offset:35040
	ds_read_b128 v[126:129], v162 offset:43744
	global_load_dwordx4 v[142:145], v[158:159], off
	v_lshl_add_u64 v[158:159], v[158:159], 0, s[72:73]
	s_waitcnt vmcnt(23)
	s_waitcnt lgkmcnt(5)
	v_mfma_f32_32x32x16_f16 v[2:17], v[130:133], v[146:149], v[2:17]
	s_waitcnt lgkmcnt(4)
	v_mfma_f32_32x32x16_f16 v[18:33], v[134:137], v[146:149], v[18:33]
	global_load_dwordx4 v[146:149], v[158:159], off
	v_lshl_add_u64 v[158:159], v[158:159], 0, s[72:73]
	s_waitcnt vmcnt(23)
	s_waitcnt lgkmcnt(3)
	v_mfma_f32_32x32x16_f16 v[2:17], v[114:117], v[150:153], v[2:17]
	s_waitcnt lgkmcnt(2)
	v_mfma_f32_32x32x16_f16 v[18:33], v[118:121], v[150:153], v[18:33]
	global_load_dwordx4 v[150:153], v[158:159], off
	v_lshl_add_u64 v[158:159], v[158:159], 0, s[72:73]
	s_waitcnt vmcnt(23)
	s_waitcnt lgkmcnt(1)
	v_mfma_f32_32x32x16_f16 v[2:17], v[122:125], v[154:157], v[2:17]
	s_waitcnt lgkmcnt(0)
	v_mfma_f32_32x32x16_f16 v[18:33], v[126:129], v[154:157], v[18:33]
	global_load_dwordx4 v[154:157], v[158:159], off
	v_lshl_add_u64 v[158:159], v[158:159], 0, s[72:73]
	s_waitcnt lgkmcnt(0)
	s_barrier
	ds_read_b128 v[114:117], v162 offset:0
	ds_read_b128 v[118:121], v162 offset:8704
	ds_read_b128 v[122:125], v162 offset:32
	ds_read_b128 v[126:129], v162 offset:8736
	ds_read_b128 v[130:133], v162 offset:64
	ds_read_b128 v[134:137], v162 offset:8768
	s_waitcnt vmcnt(23)
	s_waitcnt lgkmcnt(5)
	v_mfma_f32_32x32x16_f16 v[2:17], v[114:117], v[110:113], v[2:17]
	s_waitcnt lgkmcnt(4)
	v_mfma_f32_32x32x16_f16 v[18:33], v[118:121], v[110:113], v[18:33]
	ds_read_b128 v[114:117], v162 offset:96
	ds_read_b128 v[118:121], v162 offset:8800
	global_load_dwordx4 v[110:113], v[158:159], off
	v_lshl_add_u64 v[158:159], v[158:159], 0, s[72:73]
	s_waitcnt vmcnt(23)
	s_waitcnt lgkmcnt(5)
	v_mfma_f32_32x32x16_f16 v[2:17], v[122:125], v[90:93], v[2:17]
	s_waitcnt lgkmcnt(4)
	v_mfma_f32_32x32x16_f16 v[18:33], v[126:129], v[90:93], v[18:33]
	ds_read_b128 v[122:125], v162 offset:128
	ds_read_b128 v[126:129], v162 offset:8832
	global_load_dwordx4 v[90:93], v[158:159], off
	v_lshl_add_u64 v[158:159], v[158:159], 0, s[72:73]
	s_waitcnt vmcnt(23)
	s_waitcnt lgkmcnt(5)
	v_mfma_f32_32x32x16_f16 v[2:17], v[130:133], v[86:89], v[2:17]
	s_waitcnt lgkmcnt(4)
	v_mfma_f32_32x32x16_f16 v[18:33], v[134:137], v[86:89], v[18:33]
	ds_read_b128 v[130:133], v162 offset:160
	ds_read_b128 v[134:137], v162 offset:8864
	global_load_dwordx4 v[86:89], v[158:159], off
	v_lshl_add_u64 v[158:159], v[158:159], 0, s[72:73]
	s_waitcnt vmcnt(23)
	s_waitcnt lgkmcnt(5)
	v_mfma_f32_32x32x16_f16 v[2:17], v[114:117], v[82:85], v[2:17]
	s_waitcnt lgkmcnt(4)
	v_mfma_f32_32x32x16_f16 v[18:33], v[118:121], v[82:85], v[18:33]
	ds_read_b128 v[114:117], v162 offset:192
	ds_read_b128 v[118:121], v162 offset:8896
	global_load_dwordx4 v[82:85], v[158:159], off
	v_lshl_add_u64 v[158:159], v[158:159], 0, s[72:73]
	s_waitcnt vmcnt(23)
	s_waitcnt lgkmcnt(5)
	v_mfma_f32_32x32x16_f16 v[2:17], v[122:125], v[78:81], v[2:17]
	s_waitcnt lgkmcnt(4)
	v_mfma_f32_32x32x16_f16 v[18:33], v[126:129], v[78:81], v[18:33]
	ds_read_b128 v[122:125], v162 offset:224
	ds_read_b128 v[126:129], v162 offset:8928
	global_load_dwordx4 v[78:81], v[158:159], off
	v_lshl_add_u64 v[158:159], v[158:159], 0, s[72:73]
	s_waitcnt vmcnt(23)
	s_waitcnt lgkmcnt(5)
	v_mfma_f32_32x32x16_f16 v[2:17], v[130:133], v[74:77], v[2:17]
	s_waitcnt lgkmcnt(4)
	v_mfma_f32_32x32x16_f16 v[18:33], v[134:137], v[74:77], v[18:33]
	global_load_dwordx4 v[74:77], v[158:159], off
	v_lshl_add_u64 v[158:159], v[158:159], 0, s[72:73]
	s_waitcnt vmcnt(23)
	s_waitcnt lgkmcnt(3)
	v_mfma_f32_32x32x16_f16 v[2:17], v[114:117], v[70:73], v[2:17]
	s_waitcnt lgkmcnt(2)
	v_mfma_f32_32x32x16_f16 v[18:33], v[118:121], v[70:73], v[18:33]
	global_load_dwordx4 v[70:73], v[158:159], off
	v_lshl_add_u64 v[158:159], v[158:159], 0, s[72:73]
	s_waitcnt vmcnt(23)
	s_waitcnt lgkmcnt(1)
	v_mfma_f32_32x32x16_f16 v[2:17], v[122:125], v[66:69], v[2:17]
	s_waitcnt lgkmcnt(0)
	v_mfma_f32_32x32x16_f16 v[18:33], v[126:129], v[66:69], v[18:33]
	global_load_dwordx4 v[66:69], v[158:159], off
	v_lshl_add_u64 v[158:159], v[158:159], 0, s[72:73]
	s_waitcnt lgkmcnt(0)
	s_barrier
	ds_read_b128 v[114:117], v162 offset:17408
	ds_read_b128 v[118:121], v162 offset:26112
	ds_read_b128 v[122:125], v162 offset:17440
	ds_read_b128 v[126:129], v162 offset:26144
	ds_read_b128 v[130:133], v162 offset:17472
	ds_read_b128 v[134:137], v162 offset:26176
	s_waitcnt vmcnt(23)
	s_waitcnt lgkmcnt(5)
	v_mfma_f32_32x32x16_f16 v[2:17], v[114:117], v[62:65], v[2:17]
	s_waitcnt lgkmcnt(4)
	v_mfma_f32_32x32x16_f16 v[18:33], v[118:121], v[62:65], v[18:33]
	ds_read_b128 v[114:117], v162 offset:17504
	ds_read_b128 v[118:121], v162 offset:26208
	global_load_dwordx4 v[62:65], v[158:159], off
	v_lshl_add_u64 v[158:159], v[158:159], 0, s[72:73]
	s_waitcnt vmcnt(23)
	s_waitcnt lgkmcnt(5)
	v_mfma_f32_32x32x16_f16 v[2:17], v[122:125], v[58:61], v[2:17]
	s_waitcnt lgkmcnt(4)
	v_mfma_f32_32x32x16_f16 v[18:33], v[126:129], v[58:61], v[18:33]
	ds_read_b128 v[122:125], v162 offset:17536
	ds_read_b128 v[126:129], v162 offset:26240
	global_load_dwordx4 v[58:61], v[158:159], off
	v_lshl_add_u64 v[158:159], v[158:159], 0, s[72:73]
	s_waitcnt vmcnt(23)
	s_waitcnt lgkmcnt(5)
	v_mfma_f32_32x32x16_f16 v[2:17], v[130:133], v[54:57], v[2:17]
	s_waitcnt lgkmcnt(4)
	v_mfma_f32_32x32x16_f16 v[18:33], v[134:137], v[54:57], v[18:33]
	ds_read_b128 v[130:133], v162 offset:17568
	ds_read_b128 v[134:137], v162 offset:26272
	global_load_dwordx4 v[54:57], v[158:159], off
	v_lshl_add_u64 v[158:159], v[158:159], 0, s[72:73]
	s_waitcnt vmcnt(23)
	s_waitcnt lgkmcnt(5)
	v_mfma_f32_32x32x16_f16 v[2:17], v[114:117], v[50:53], v[2:17]
	s_waitcnt lgkmcnt(4)
	v_mfma_f32_32x32x16_f16 v[18:33], v[118:121], v[50:53], v[18:33]
	ds_read_b128 v[114:117], v162 offset:17600
	ds_read_b128 v[118:121], v162 offset:26304
	global_load_dwordx4 v[50:53], v[158:159], off
	v_lshl_add_u64 v[158:159], v[158:159], 0, s[72:73]
	s_waitcnt vmcnt(23)
	s_waitcnt lgkmcnt(5)
	v_mfma_f32_32x32x16_f16 v[2:17], v[122:125], v[46:49], v[2:17]
	s_waitcnt lgkmcnt(4)
	v_mfma_f32_32x32x16_f16 v[18:33], v[126:129], v[46:49], v[18:33]
	ds_read_b128 v[122:125], v162 offset:17632
	ds_read_b128 v[126:129], v162 offset:26336
	global_load_dwordx4 v[46:49], v[158:159], off
	v_lshl_add_u64 v[158:159], v[158:159], 0, s[72:73]
	s_waitcnt vmcnt(23)
	s_waitcnt lgkmcnt(5)
	v_mfma_f32_32x32x16_f16 v[2:17], v[130:133], v[42:45], v[2:17]
	s_waitcnt lgkmcnt(4)
	v_mfma_f32_32x32x16_f16 v[18:33], v[134:137], v[42:45], v[18:33]
	global_load_dwordx4 v[42:45], v[158:159], off
	v_lshl_add_u64 v[158:159], v[158:159], 0, s[72:73]
	s_waitcnt vmcnt(23)
	s_waitcnt lgkmcnt(3)
	v_mfma_f32_32x32x16_f16 v[2:17], v[114:117], v[38:41], v[2:17]
	s_waitcnt lgkmcnt(2)
	v_mfma_f32_32x32x16_f16 v[18:33], v[118:121], v[38:41], v[18:33]
	global_load_dwordx4 v[38:41], v[158:159], off
	v_lshl_add_u64 v[158:159], v[158:159], 0, s[72:73]
	s_waitcnt vmcnt(23)
	s_waitcnt lgkmcnt(1)
	v_mfma_f32_32x32x16_f16 v[2:17], v[122:125], v[34:37], v[2:17]
	s_waitcnt lgkmcnt(0)
	v_mfma_f32_32x32x16_f16 v[18:33], v[126:129], v[34:37], v[18:33]
	global_load_dwordx4 v[34:37], v[158:159], off
	v_lshl_add_u64 v[158:159], v[158:159], 0, s[72:73]
	s_waitcnt lgkmcnt(0)
	s_barrier
	ds_read_b128 v[114:117], v162 offset:34816
	ds_read_b128 v[118:121], v162 offset:43520
	ds_read_b128 v[122:125], v162 offset:34848
	ds_read_b128 v[126:129], v162 offset:43552
	ds_read_b128 v[130:133], v162 offset:34880
	ds_read_b128 v[134:137], v162 offset:43584
	s_waitcnt vmcnt(23)
	s_waitcnt lgkmcnt(5)
	v_mfma_f32_32x32x16_f16 v[2:17], v[114:117], v[94:97], v[2:17]
	s_waitcnt lgkmcnt(4)
	v_mfma_f32_32x32x16_f16 v[18:33], v[118:121], v[94:97], v[18:33]
	ds_read_b128 v[114:117], v162 offset:34912
	ds_read_b128 v[118:121], v162 offset:43616
	global_load_dwordx4 v[94:97], v[158:159], off
	v_lshl_add_u64 v[158:159], v[158:159], 0, s[72:73]
	s_waitcnt vmcnt(23)
	s_waitcnt lgkmcnt(5)
	v_mfma_f32_32x32x16_f16 v[2:17], v[122:125], v[98:101], v[2:17]
	s_waitcnt lgkmcnt(4)
	v_mfma_f32_32x32x16_f16 v[18:33], v[126:129], v[98:101], v[18:33]
	ds_read_b128 v[122:125], v162 offset:34944
	ds_read_b128 v[126:129], v162 offset:43648
	global_load_dwordx4 v[98:101], v[158:159], off
	v_lshl_add_u64 v[158:159], v[158:159], 0, s[72:73]
	s_waitcnt vmcnt(23)
	s_waitcnt lgkmcnt(5)
	v_mfma_f32_32x32x16_f16 v[2:17], v[130:133], v[102:105], v[2:17]
	s_waitcnt lgkmcnt(4)
	v_mfma_f32_32x32x16_f16 v[18:33], v[134:137], v[102:105], v[18:33]
	ds_read_b128 v[130:133], v162 offset:34976
	ds_read_b128 v[134:137], v162 offset:43680
	global_load_dwordx4 v[102:105], v[158:159], off
	v_lshl_add_u64 v[158:159], v[158:159], 0, s[72:73]
	s_waitcnt vmcnt(23)
	s_waitcnt lgkmcnt(5)
	v_mfma_f32_32x32x16_f16 v[2:17], v[114:117], v[106:109], v[2:17]
	s_waitcnt lgkmcnt(4)
	v_mfma_f32_32x32x16_f16 v[18:33], v[118:121], v[106:109], v[18:33]
	ds_read_b128 v[114:117], v162 offset:35008
	ds_read_b128 v[118:121], v162 offset:43712
	global_load_dwordx4 v[106:109], v[158:159], off
	v_lshl_add_u64 v[158:159], v[158:159], 0, s[72:73]
	s_waitcnt vmcnt(23)
	s_waitcnt lgkmcnt(5)
	v_mfma_f32_32x32x16_f16 v[2:17], v[122:125], v[142:145], v[2:17]
	s_waitcnt lgkmcnt(4)
	v_mfma_f32_32x32x16_f16 v[18:33], v[126:129], v[142:145], v[18:33]
	ds_read_b128 v[122:125], v162 offset:35040
	ds_read_b128 v[126:129], v162 offset:43744
	global_load_dwordx4 v[142:145], v[158:159], off
	v_lshl_add_u64 v[158:159], v[158:159], 0, s[72:73]
	s_waitcnt vmcnt(23)
	s_waitcnt lgkmcnt(5)
	v_mfma_f32_32x32x16_f16 v[2:17], v[130:133], v[146:149], v[2:17]
	s_waitcnt lgkmcnt(4)
	v_mfma_f32_32x32x16_f16 v[18:33], v[134:137], v[146:149], v[18:33]
	global_load_dwordx4 v[146:149], v[158:159], off
	v_lshl_add_u64 v[158:159], v[158:159], 0, s[72:73]
	s_waitcnt vmcnt(23)
	s_waitcnt lgkmcnt(3)
	v_mfma_f32_32x32x16_f16 v[2:17], v[114:117], v[150:153], v[2:17]
	s_waitcnt lgkmcnt(2)
	v_mfma_f32_32x32x16_f16 v[18:33], v[118:121], v[150:153], v[18:33]
	global_load_dwordx4 v[150:153], v[158:159], off
	v_lshl_add_u64 v[158:159], v[158:159], 0, s[72:73]
	s_waitcnt vmcnt(23)
	s_waitcnt lgkmcnt(1)
	v_mfma_f32_32x32x16_f16 v[2:17], v[122:125], v[154:157], v[2:17]
	s_waitcnt lgkmcnt(0)
	v_mfma_f32_32x32x16_f16 v[18:33], v[126:129], v[154:157], v[18:33]
	global_load_dwordx4 v[154:157], v[158:159], off
	v_lshl_add_u64 v[158:159], v[158:159], 0, s[72:73]
	s_waitcnt lgkmcnt(0)
	s_barrier
	ds_read_b128 v[114:117], v162 offset:0
	ds_read_b128 v[118:121], v162 offset:8704
	ds_read_b128 v[122:125], v162 offset:32
	ds_read_b128 v[126:129], v162 offset:8736
	ds_read_b128 v[130:133], v162 offset:64
	ds_read_b128 v[134:137], v162 offset:8768
	s_waitcnt vmcnt(23)
	s_waitcnt lgkmcnt(5)
	v_mfma_f32_32x32x16_f16 v[2:17], v[114:117], v[110:113], v[2:17]
	s_waitcnt lgkmcnt(4)
	v_mfma_f32_32x32x16_f16 v[18:33], v[118:121], v[110:113], v[18:33]
	ds_read_b128 v[114:117], v162 offset:96
	ds_read_b128 v[118:121], v162 offset:8800
	global_load_dwordx4 v[110:113], v[158:159], off
	v_lshl_add_u64 v[158:159], v[158:159], 0, s[72:73]
	s_waitcnt vmcnt(23)
	s_waitcnt lgkmcnt(5)
	v_mfma_f32_32x32x16_f16 v[2:17], v[122:125], v[90:93], v[2:17]
	s_waitcnt lgkmcnt(4)
	v_mfma_f32_32x32x16_f16 v[18:33], v[126:129], v[90:93], v[18:33]
	ds_read_b128 v[122:125], v162 offset:128
	ds_read_b128 v[126:129], v162 offset:8832
	global_load_dwordx4 v[90:93], v[158:159], off
	v_lshl_add_u64 v[158:159], v[158:159], 0, s[72:73]
	s_waitcnt vmcnt(23)
	s_waitcnt lgkmcnt(5)
	v_mfma_f32_32x32x16_f16 v[2:17], v[130:133], v[86:89], v[2:17]
	s_waitcnt lgkmcnt(4)
	v_mfma_f32_32x32x16_f16 v[18:33], v[134:137], v[86:89], v[18:33]
	ds_read_b128 v[130:133], v162 offset:160
	ds_read_b128 v[134:137], v162 offset:8864
	global_load_dwordx4 v[86:89], v[158:159], off
	v_lshl_add_u64 v[158:159], v[158:159], 0, s[72:73]
	s_waitcnt vmcnt(23)
	s_waitcnt lgkmcnt(5)
	v_mfma_f32_32x32x16_f16 v[2:17], v[114:117], v[82:85], v[2:17]
	s_waitcnt lgkmcnt(4)
	v_mfma_f32_32x32x16_f16 v[18:33], v[118:121], v[82:85], v[18:33]
	ds_read_b128 v[114:117], v162 offset:192
	ds_read_b128 v[118:121], v162 offset:8896
	global_load_dwordx4 v[82:85], v[158:159], off
	v_lshl_add_u64 v[158:159], v[158:159], 0, s[72:73]
	s_waitcnt vmcnt(23)
	s_waitcnt lgkmcnt(5)
	v_mfma_f32_32x32x16_f16 v[2:17], v[122:125], v[78:81], v[2:17]
	s_waitcnt lgkmcnt(4)
	v_mfma_f32_32x32x16_f16 v[18:33], v[126:129], v[78:81], v[18:33]
	ds_read_b128 v[122:125], v162 offset:224
	ds_read_b128 v[126:129], v162 offset:8928
	global_load_dwordx4 v[78:81], v[158:159], off
	v_lshl_add_u64 v[158:159], v[158:159], 0, s[72:73]
	s_waitcnt vmcnt(23)
	s_waitcnt lgkmcnt(5)
	v_mfma_f32_32x32x16_f16 v[2:17], v[130:133], v[74:77], v[2:17]
	s_waitcnt lgkmcnt(4)
	v_mfma_f32_32x32x16_f16 v[18:33], v[134:137], v[74:77], v[18:33]
	global_load_dwordx4 v[74:77], v[158:159], off
	v_lshl_add_u64 v[158:159], v[158:159], 0, s[72:73]
	s_waitcnt vmcnt(23)
	s_waitcnt lgkmcnt(3)
	v_mfma_f32_32x32x16_f16 v[2:17], v[114:117], v[70:73], v[2:17]
	s_waitcnt lgkmcnt(2)
	v_mfma_f32_32x32x16_f16 v[18:33], v[118:121], v[70:73], v[18:33]
	global_load_dwordx4 v[70:73], v[158:159], off
	v_lshl_add_u64 v[158:159], v[158:159], 0, s[72:73]
	s_waitcnt vmcnt(23)
	s_waitcnt lgkmcnt(1)
	v_mfma_f32_32x32x16_f16 v[2:17], v[122:125], v[66:69], v[2:17]
	s_waitcnt lgkmcnt(0)
	v_mfma_f32_32x32x16_f16 v[18:33], v[126:129], v[66:69], v[18:33]
	global_load_dwordx4 v[66:69], v[158:159], off
	v_lshl_add_u64 v[158:159], v[158:159], 0, s[72:73]
	s_waitcnt lgkmcnt(0)
	s_barrier
	ds_read_b128 v[114:117], v162 offset:17408
	ds_read_b128 v[118:121], v162 offset:26112
	ds_read_b128 v[122:125], v162 offset:17440
	ds_read_b128 v[126:129], v162 offset:26144
	ds_read_b128 v[130:133], v162 offset:17472
	ds_read_b128 v[134:137], v162 offset:26176
	s_waitcnt vmcnt(23)
	s_waitcnt lgkmcnt(5)
	v_mfma_f32_32x32x16_f16 v[2:17], v[114:117], v[62:65], v[2:17]
	s_waitcnt lgkmcnt(4)
	v_mfma_f32_32x32x16_f16 v[18:33], v[118:121], v[62:65], v[18:33]
	ds_read_b128 v[114:117], v162 offset:17504
	ds_read_b128 v[118:121], v162 offset:26208
	global_load_dwordx4 v[62:65], v[158:159], off
	v_lshl_add_u64 v[158:159], v[158:159], 0, s[72:73]
	s_waitcnt vmcnt(23)
	s_waitcnt lgkmcnt(5)
	v_mfma_f32_32x32x16_f16 v[2:17], v[122:125], v[58:61], v[2:17]
	s_waitcnt lgkmcnt(4)
	v_mfma_f32_32x32x16_f16 v[18:33], v[126:129], v[58:61], v[18:33]
	ds_read_b128 v[122:125], v162 offset:17536
	ds_read_b128 v[126:129], v162 offset:26240
	global_load_dwordx4 v[58:61], v[158:159], off
	v_lshl_add_u64 v[158:159], v[158:159], 0, s[72:73]
	s_waitcnt vmcnt(23)
	s_waitcnt lgkmcnt(5)
	v_mfma_f32_32x32x16_f16 v[2:17], v[130:133], v[54:57], v[2:17]
	s_waitcnt lgkmcnt(4)
	v_mfma_f32_32x32x16_f16 v[18:33], v[134:137], v[54:57], v[18:33]
	ds_read_b128 v[130:133], v162 offset:17568
	ds_read_b128 v[134:137], v162 offset:26272
	global_load_dwordx4 v[54:57], v[158:159], off
	v_lshl_add_u64 v[158:159], v[158:159], 0, s[72:73]
	s_waitcnt vmcnt(23)
	s_waitcnt lgkmcnt(5)
	v_mfma_f32_32x32x16_f16 v[2:17], v[114:117], v[50:53], v[2:17]
	s_waitcnt lgkmcnt(4)
	v_mfma_f32_32x32x16_f16 v[18:33], v[118:121], v[50:53], v[18:33]
	ds_read_b128 v[114:117], v162 offset:17600
	ds_read_b128 v[118:121], v162 offset:26304
	global_load_dwordx4 v[50:53], v[158:159], off
	v_lshl_add_u64 v[158:159], v[158:159], 0, s[72:73]
	s_waitcnt vmcnt(23)
	s_waitcnt lgkmcnt(5)
	v_mfma_f32_32x32x16_f16 v[2:17], v[122:125], v[46:49], v[2:17]
	s_waitcnt lgkmcnt(4)
	v_mfma_f32_32x32x16_f16 v[18:33], v[126:129], v[46:49], v[18:33]
	ds_read_b128 v[122:125], v162 offset:17632
	ds_read_b128 v[126:129], v162 offset:26336
	global_load_dwordx4 v[46:49], v[158:159], off
	v_lshl_add_u64 v[158:159], v[158:159], 0, s[72:73]
	s_waitcnt vmcnt(23)
	s_waitcnt lgkmcnt(5)
	v_mfma_f32_32x32x16_f16 v[2:17], v[130:133], v[42:45], v[2:17]
	s_waitcnt lgkmcnt(4)
	v_mfma_f32_32x32x16_f16 v[18:33], v[134:137], v[42:45], v[18:33]
	global_load_dwordx4 v[42:45], v[158:159], off
	v_lshl_add_u64 v[158:159], v[158:159], 0, s[72:73]
	s_waitcnt vmcnt(23)
	s_waitcnt lgkmcnt(3)
	v_mfma_f32_32x32x16_f16 v[2:17], v[114:117], v[38:41], v[2:17]
	s_waitcnt lgkmcnt(2)
	v_mfma_f32_32x32x16_f16 v[18:33], v[118:121], v[38:41], v[18:33]
	global_load_dwordx4 v[38:41], v[158:159], off
	v_lshl_add_u64 v[158:159], v[158:159], 0, s[72:73]
	s_waitcnt vmcnt(23)
	s_waitcnt lgkmcnt(1)
	v_mfma_f32_32x32x16_f16 v[2:17], v[122:125], v[34:37], v[2:17]
	s_waitcnt lgkmcnt(0)
	v_mfma_f32_32x32x16_f16 v[18:33], v[126:129], v[34:37], v[18:33]
	global_load_dwordx4 v[34:37], v[158:159], off
	v_lshl_add_u64 v[158:159], v[158:159], 0, s[72:73]
	s_waitcnt lgkmcnt(0)
	s_barrier
	ds_read_b128 v[114:117], v162 offset:34816
	ds_read_b128 v[118:121], v162 offset:43520
	ds_read_b128 v[122:125], v162 offset:34848
	ds_read_b128 v[126:129], v162 offset:43552
	ds_read_b128 v[130:133], v162 offset:34880
	ds_read_b128 v[134:137], v162 offset:43584
	s_waitcnt vmcnt(23)
	s_waitcnt lgkmcnt(5)
	v_mfma_f32_32x32x16_f16 v[2:17], v[114:117], v[94:97], v[2:17]
	s_waitcnt lgkmcnt(4)
	v_mfma_f32_32x32x16_f16 v[18:33], v[118:121], v[94:97], v[18:33]
	ds_read_b128 v[114:117], v162 offset:34912
	ds_read_b128 v[118:121], v162 offset:43616
	global_load_dwordx4 v[94:97], v[158:159], off
	v_lshl_add_u64 v[158:159], v[158:159], 0, s[72:73]
	s_waitcnt vmcnt(23)
	s_waitcnt lgkmcnt(5)
	v_mfma_f32_32x32x16_f16 v[2:17], v[122:125], v[98:101], v[2:17]
	s_waitcnt lgkmcnt(4)
	v_mfma_f32_32x32x16_f16 v[18:33], v[126:129], v[98:101], v[18:33]
	ds_read_b128 v[122:125], v162 offset:34944
	ds_read_b128 v[126:129], v162 offset:43648
	global_load_dwordx4 v[98:101], v[158:159], off
	v_lshl_add_u64 v[158:159], v[158:159], 0, s[72:73]
	s_waitcnt vmcnt(23)
	s_waitcnt lgkmcnt(5)
	v_mfma_f32_32x32x16_f16 v[2:17], v[130:133], v[102:105], v[2:17]
	s_waitcnt lgkmcnt(4)
	v_mfma_f32_32x32x16_f16 v[18:33], v[134:137], v[102:105], v[18:33]
	ds_read_b128 v[130:133], v162 offset:34976
	ds_read_b128 v[134:137], v162 offset:43680
	global_load_dwordx4 v[102:105], v[158:159], off
	v_lshl_add_u64 v[158:159], v[158:159], 0, s[72:73]
	s_waitcnt vmcnt(23)
	s_waitcnt lgkmcnt(5)
	v_mfma_f32_32x32x16_f16 v[2:17], v[114:117], v[106:109], v[2:17]
	s_waitcnt lgkmcnt(4)
	v_mfma_f32_32x32x16_f16 v[18:33], v[118:121], v[106:109], v[18:33]
	ds_read_b128 v[114:117], v162 offset:35008
	ds_read_b128 v[118:121], v162 offset:43712
	global_load_dwordx4 v[106:109], v[158:159], off
	v_lshl_add_u64 v[158:159], v[158:159], 0, s[72:73]
	s_waitcnt vmcnt(23)
	s_waitcnt lgkmcnt(5)
	v_mfma_f32_32x32x16_f16 v[2:17], v[122:125], v[142:145], v[2:17]
	s_waitcnt lgkmcnt(4)
	v_mfma_f32_32x32x16_f16 v[18:33], v[126:129], v[142:145], v[18:33]
	ds_read_b128 v[122:125], v162 offset:35040
	ds_read_b128 v[126:129], v162 offset:43744
	global_load_dwordx4 v[142:145], v[158:159], off
	v_lshl_add_u64 v[158:159], v[158:159], 0, s[72:73]
	s_waitcnt vmcnt(23)
	s_waitcnt lgkmcnt(5)
	v_mfma_f32_32x32x16_f16 v[2:17], v[130:133], v[146:149], v[2:17]
	s_waitcnt lgkmcnt(4)
	v_mfma_f32_32x32x16_f16 v[18:33], v[134:137], v[146:149], v[18:33]
	global_load_dwordx4 v[146:149], v[158:159], off
	v_lshl_add_u64 v[158:159], v[158:159], 0, s[72:73]
	s_waitcnt vmcnt(23)
	s_waitcnt lgkmcnt(3)
	v_mfma_f32_32x32x16_f16 v[2:17], v[114:117], v[150:153], v[2:17]
	s_waitcnt lgkmcnt(2)
	v_mfma_f32_32x32x16_f16 v[18:33], v[118:121], v[150:153], v[18:33]
	global_load_dwordx4 v[150:153], v[158:159], off
	v_lshl_add_u64 v[158:159], v[158:159], 0, s[72:73]
	s_waitcnt vmcnt(23)
	s_waitcnt lgkmcnt(1)
	v_mfma_f32_32x32x16_f16 v[2:17], v[122:125], v[154:157], v[2:17]
	s_waitcnt lgkmcnt(0)
	v_mfma_f32_32x32x16_f16 v[18:33], v[126:129], v[154:157], v[18:33]
	global_load_dwordx4 v[154:157], v[158:159], off
	v_lshl_add_u64 v[158:159], v[158:159], 0, s[72:73]
	s_waitcnt lgkmcnt(0)
	s_barrier
	ds_read_b128 v[114:117], v162 offset:0
	ds_read_b128 v[118:121], v162 offset:8704
	ds_read_b128 v[122:125], v162 offset:32
	ds_read_b128 v[126:129], v162 offset:8736
	ds_read_b128 v[130:133], v162 offset:64
	ds_read_b128 v[134:137], v162 offset:8768
	s_waitcnt vmcnt(23)
	s_waitcnt lgkmcnt(5)
	v_mfma_f32_32x32x16_f16 v[2:17], v[114:117], v[110:113], v[2:17]
	s_waitcnt lgkmcnt(4)
	v_mfma_f32_32x32x16_f16 v[18:33], v[118:121], v[110:113], v[18:33]
	ds_read_b128 v[114:117], v162 offset:96
	ds_read_b128 v[118:121], v162 offset:8800
	s_waitcnt vmcnt(22)
	s_waitcnt lgkmcnt(5)
	v_mfma_f32_32x32x16_f16 v[2:17], v[122:125], v[90:93], v[2:17]
	s_waitcnt lgkmcnt(4)
	v_mfma_f32_32x32x16_f16 v[18:33], v[126:129], v[90:93], v[18:33]
	ds_read_b128 v[122:125], v162 offset:128
	ds_read_b128 v[126:129], v162 offset:8832
	s_waitcnt vmcnt(21)
	s_waitcnt lgkmcnt(5)
	v_mfma_f32_32x32x16_f16 v[2:17], v[130:133], v[86:89], v[2:17]
	s_waitcnt lgkmcnt(4)
	v_mfma_f32_32x32x16_f16 v[18:33], v[134:137], v[86:89], v[18:33]
	ds_read_b128 v[130:133], v162 offset:160
	ds_read_b128 v[134:137], v162 offset:8864
	s_waitcnt vmcnt(20)
	s_waitcnt lgkmcnt(5)
	v_mfma_f32_32x32x16_f16 v[2:17], v[114:117], v[82:85], v[2:17]
	s_waitcnt lgkmcnt(4)
	v_mfma_f32_32x32x16_f16 v[18:33], v[118:121], v[82:85], v[18:33]
	ds_read_b128 v[114:117], v162 offset:192
	ds_read_b128 v[118:121], v162 offset:8896
	s_waitcnt vmcnt(19)
	s_waitcnt lgkmcnt(5)
	v_mfma_f32_32x32x16_f16 v[2:17], v[122:125], v[78:81], v[2:17]
	s_waitcnt lgkmcnt(4)
	v_mfma_f32_32x32x16_f16 v[18:33], v[126:129], v[78:81], v[18:33]
	ds_read_b128 v[122:125], v162 offset:224
	ds_read_b128 v[126:129], v162 offset:8928
	s_waitcnt vmcnt(18)
	s_waitcnt lgkmcnt(5)
	v_mfma_f32_32x32x16_f16 v[2:17], v[130:133], v[74:77], v[2:17]
	s_waitcnt lgkmcnt(4)
	v_mfma_f32_32x32x16_f16 v[18:33], v[134:137], v[74:77], v[18:33]
	s_waitcnt vmcnt(17)
	s_waitcnt lgkmcnt(3)
	v_mfma_f32_32x32x16_f16 v[2:17], v[114:117], v[70:73], v[2:17]
	s_waitcnt lgkmcnt(2)
	v_mfma_f32_32x32x16_f16 v[18:33], v[118:121], v[70:73], v[18:33]
	s_waitcnt vmcnt(16)
	s_waitcnt lgkmcnt(1)
	v_mfma_f32_32x32x16_f16 v[2:17], v[122:125], v[66:69], v[2:17]
	s_waitcnt lgkmcnt(0)
	v_mfma_f32_32x32x16_f16 v[18:33], v[126:129], v[66:69], v[18:33]
	s_waitcnt lgkmcnt(0)
	s_barrier
	ds_read_b128 v[114:117], v162 offset:17408
	ds_read_b128 v[118:121], v162 offset:26112
	ds_read_b128 v[122:125], v162 offset:17440
	ds_read_b128 v[126:129], v162 offset:26144
	ds_read_b128 v[130:133], v162 offset:17472
	ds_read_b128 v[134:137], v162 offset:26176
	s_waitcnt vmcnt(15)
	s_waitcnt lgkmcnt(5)
	v_mfma_f32_32x32x16_f16 v[2:17], v[114:117], v[62:65], v[2:17]
	s_waitcnt lgkmcnt(4)
	v_mfma_f32_32x32x16_f16 v[18:33], v[118:121], v[62:65], v[18:33]
	ds_read_b128 v[114:117], v162 offset:17504
	ds_read_b128 v[118:121], v162 offset:26208
	s_waitcnt vmcnt(14)
	s_waitcnt lgkmcnt(5)
	v_mfma_f32_32x32x16_f16 v[2:17], v[122:125], v[58:61], v[2:17]
	s_waitcnt lgkmcnt(4)
	v_mfma_f32_32x32x16_f16 v[18:33], v[126:129], v[58:61], v[18:33]
	ds_read_b128 v[122:125], v162 offset:17536
	ds_read_b128 v[126:129], v162 offset:26240
	s_waitcnt vmcnt(13)
	s_waitcnt lgkmcnt(5)
	v_mfma_f32_32x32x16_f16 v[2:17], v[130:133], v[54:57], v[2:17]
	s_waitcnt lgkmcnt(4)
	v_mfma_f32_32x32x16_f16 v[18:33], v[134:137], v[54:57], v[18:33]
	ds_read_b128 v[130:133], v162 offset:17568
	ds_read_b128 v[134:137], v162 offset:26272
	s_waitcnt vmcnt(12)
	s_waitcnt lgkmcnt(5)
	v_mfma_f32_32x32x16_f16 v[2:17], v[114:117], v[50:53], v[2:17]
	s_waitcnt lgkmcnt(4)
	v_mfma_f32_32x32x16_f16 v[18:33], v[118:121], v[50:53], v[18:33]
	ds_read_b128 v[114:117], v162 offset:17600
	ds_read_b128 v[118:121], v162 offset:26304
	s_waitcnt vmcnt(11)
	s_waitcnt lgkmcnt(5)
	v_mfma_f32_32x32x16_f16 v[2:17], v[122:125], v[46:49], v[2:17]
	s_waitcnt lgkmcnt(4)
	v_mfma_f32_32x32x16_f16 v[18:33], v[126:129], v[46:49], v[18:33]
	ds_read_b128 v[122:125], v162 offset:17632
	ds_read_b128 v[126:129], v162 offset:26336
	s_waitcnt vmcnt(10)
	s_waitcnt lgkmcnt(5)
	v_mfma_f32_32x32x16_f16 v[2:17], v[130:133], v[42:45], v[2:17]
	s_waitcnt lgkmcnt(4)
	v_mfma_f32_32x32x16_f16 v[18:33], v[134:137], v[42:45], v[18:33]
	s_waitcnt vmcnt(9)
	s_waitcnt lgkmcnt(3)
	v_mfma_f32_32x32x16_f16 v[2:17], v[114:117], v[38:41], v[2:17]
	s_waitcnt lgkmcnt(2)
	v_mfma_f32_32x32x16_f16 v[18:33], v[118:121], v[38:41], v[18:33]
	s_waitcnt vmcnt(8)
	s_waitcnt lgkmcnt(1)
	v_mfma_f32_32x32x16_f16 v[2:17], v[122:125], v[34:37], v[2:17]
	s_waitcnt lgkmcnt(0)
	v_mfma_f32_32x32x16_f16 v[18:33], v[126:129], v[34:37], v[18:33]
	s_waitcnt lgkmcnt(0)
	s_barrier
	ds_read_b128 v[114:117], v162 offset:34816
	ds_read_b128 v[118:121], v162 offset:43520
	ds_read_b128 v[122:125], v162 offset:34848
	ds_read_b128 v[126:129], v162 offset:43552
	ds_read_b128 v[130:133], v162 offset:34880
	ds_read_b128 v[134:137], v162 offset:43584
	s_waitcnt vmcnt(7)
	s_waitcnt lgkmcnt(5)
	v_mfma_f32_32x32x16_f16 v[2:17], v[114:117], v[94:97], v[2:17]
	s_waitcnt lgkmcnt(4)
	v_mfma_f32_32x32x16_f16 v[18:33], v[118:121], v[94:97], v[18:33]
	ds_read_b128 v[114:117], v162 offset:34912
	ds_read_b128 v[118:121], v162 offset:43616
	s_waitcnt vmcnt(6)
	s_waitcnt lgkmcnt(5)
	v_mfma_f32_32x32x16_f16 v[2:17], v[122:125], v[98:101], v[2:17]
	s_waitcnt lgkmcnt(4)
	v_mfma_f32_32x32x16_f16 v[18:33], v[126:129], v[98:101], v[18:33]
	ds_read_b128 v[122:125], v162 offset:34944
	ds_read_b128 v[126:129], v162 offset:43648
	s_waitcnt vmcnt(5)
	s_waitcnt lgkmcnt(5)
	v_mfma_f32_32x32x16_f16 v[2:17], v[130:133], v[102:105], v[2:17]
	s_waitcnt lgkmcnt(4)
	v_mfma_f32_32x32x16_f16 v[18:33], v[134:137], v[102:105], v[18:33]
	ds_read_b128 v[130:133], v162 offset:34976
	ds_read_b128 v[134:137], v162 offset:43680
	s_waitcnt vmcnt(4)
	s_waitcnt lgkmcnt(5)
	v_mfma_f32_32x32x16_f16 v[2:17], v[114:117], v[106:109], v[2:17]
	s_waitcnt lgkmcnt(4)
	v_mfma_f32_32x32x16_f16 v[18:33], v[118:121], v[106:109], v[18:33]
	ds_read_b128 v[114:117], v162 offset:35008
	ds_read_b128 v[118:121], v162 offset:43712
	s_waitcnt vmcnt(3)
	s_waitcnt lgkmcnt(5)
	v_mfma_f32_32x32x16_f16 v[2:17], v[122:125], v[142:145], v[2:17]
	s_waitcnt lgkmcnt(4)
	v_mfma_f32_32x32x16_f16 v[18:33], v[126:129], v[142:145], v[18:33]
	ds_read_b128 v[122:125], v162 offset:35040
	ds_read_b128 v[126:129], v162 offset:43744
	s_waitcnt vmcnt(2)
	s_waitcnt lgkmcnt(5)
	v_mfma_f32_32x32x16_f16 v[2:17], v[130:133], v[146:149], v[2:17]
	s_waitcnt lgkmcnt(4)
	v_mfma_f32_32x32x16_f16 v[18:33], v[134:137], v[146:149], v[18:33]
	s_waitcnt vmcnt(1)
	s_waitcnt lgkmcnt(3)
	v_mfma_f32_32x32x16_f16 v[2:17], v[114:117], v[150:153], v[2:17]
	s_waitcnt lgkmcnt(2)
	v_mfma_f32_32x32x16_f16 v[18:33], v[118:121], v[150:153], v[18:33]
	s_waitcnt vmcnt(0)
	s_waitcnt lgkmcnt(1)
	v_mfma_f32_32x32x16_f16 v[2:17], v[122:125], v[154:157], v[2:17]
	s_waitcnt lgkmcnt(0)
	v_mfma_f32_32x32x16_f16 v[18:33], v[126:129], v[154:157], v[18:33]
	s_waitcnt lgkmcnt(0)
	s_barrier
	s_mov_b32 s2, 0x3d800000
	v_mul_u32_u24_e32 v1, 0x420, v1
	v_or_b32_e32 v34, v161, v160
	v_lshlrev_b32_e32 v34, 1, v34
	v_lshl_add_u32 v1, v1, 1, v34
	s_nop 7
	s_nop 7
	v_fma_mixlo_f16 v2, v2, s2, 0
	ds_write_b16 v1, v2
	v_fma_mixlo_f16 v2, v18, s2, 0
	ds_write_b16 v1, v2 offset:16896
	v_fma_mixlo_f16 v2, v3, s2, 0
	ds_write_b16 v1, v2 offset:528
	v_fma_mixlo_f16 v2, v19, s2, 0
	ds_write_b16 v1, v2 offset:17424
	v_fma_mixlo_f16 v2, v4, s2, 0
	ds_write_b16 v1, v2 offset:1056
	v_fma_mixlo_f16 v2, v20, s2, 0
	ds_write_b16 v1, v2 offset:17952
	v_fma_mixlo_f16 v2, v5, s2, 0
	ds_write_b16 v1, v2 offset:1584
	v_fma_mixlo_f16 v2, v21, s2, 0
	ds_write_b16 v1, v2 offset:18480
	v_fma_mixlo_f16 v2, v6, s2, 0
	ds_write_b16 v1, v2 offset:4224
	v_fma_mixlo_f16 v2, v22, s2, 0
	ds_write_b16 v1, v2 offset:21120
	v_fma_mixlo_f16 v2, v7, s2, 0
	ds_write_b16 v1, v2 offset:4752
	v_fma_mixlo_f16 v2, v23, s2, 0
	ds_write_b16 v1, v2 offset:21648
	v_fma_mixlo_f16 v2, v8, s2, 0
	ds_write_b16 v1, v2 offset:5280
	v_fma_mixlo_f16 v2, v24, s2, 0
	ds_write_b16 v1, v2 offset:22176
	v_fma_mixlo_f16 v2, v9, s2, 0
	ds_write_b16 v1, v2 offset:5808
	v_fma_mixlo_f16 v2, v25, s2, 0
	ds_write_b16 v1, v2 offset:22704
	v_fma_mixlo_f16 v2, v10, s2, 0
	ds_write_b16 v1, v2 offset:8448
	v_fma_mixlo_f16 v2, v26, s2, 0
	ds_write_b16 v1, v2 offset:25344
	v_fma_mixlo_f16 v2, v11, s2, 0
	ds_write_b16 v1, v2 offset:8976
	v_fma_mixlo_f16 v2, v27, s2, 0
	ds_write_b16 v1, v2 offset:25872
	v_fma_mixlo_f16 v2, v12, s2, 0
	ds_write_b16 v1, v2 offset:9504
	v_fma_mixlo_f16 v2, v28, s2, 0
	ds_write_b16 v1, v2 offset:26400
	v_fma_mixlo_f16 v2, v13, s2, 0
	ds_write_b16 v1, v2 offset:10032
	v_fma_mixlo_f16 v2, v29, s2, 0
	ds_write_b16 v1, v2 offset:26928
	v_fma_mixlo_f16 v2, v14, s2, 0
	ds_write_b16 v1, v2 offset:12672
	v_fma_mixlo_f16 v2, v30, s2, 0
	ds_write_b16 v1, v2 offset:29568
	v_fma_mixlo_f16 v2, v15, s2, 0
	ds_write_b16 v1, v2 offset:13200
	v_fma_mixlo_f16 v2, v31, s2, 0
	ds_write_b16 v1, v2 offset:30096
	v_fma_mixlo_f16 v2, v16, s2, 0
	ds_write_b16 v1, v2 offset:13728
	v_fma_mixlo_f16 v2, v32, s2, 0
	ds_write_b16 v1, v2 offset:30624
	v_fma_mixlo_f16 v2, v17, s2, 0
	ds_write_b16 v1, v2 offset:14256
	v_fma_mixlo_f16 v2, v33, s2, 0
	ds_write_b16 v1, v2 offset:31152
	v_lshrrev_b32_e32 v1, 3, v0
	v_lshlrev_b32_e32 v0, 4, v0
	v_and_b32_e32 v4, 0x70, v0
	s_movk_i32 s2, 0x210
	v_mad_u32_u24 v12, v1, s2, v4
	s_ashr_i32 s2, s8, 31
	s_waitcnt lgkmcnt(0)
	s_barrier
	v_or_b32_e32 v6, s8, v1
	v_mov_b32_e32 v7, s2
	v_mov_b32_e32 v5, 0
	ds_read_b128 v[0:3], v12
	v_lshl_add_u64 v[4:5], s[16:17], 0, v[4:5]
	v_lshlrev_b64 v[6:7], 7, v[6:7]
	v_lshl_add_u64 v[8:9], v[4:5], 0, v[6:7]
	ds_read_b128 v[4:7], v12 offset:128
	s_mov_b32 s2, 0x200000
	s_waitcnt lgkmcnt(1)
	global_store_dwordx4 v[8:9], v[0:3], off
	s_nop 1
	v_add_co_u32_e32 v0, vcc, s2, v8
	s_nop 1
	v_addc_co_u32_e32 v1, vcc, 0, v9, vcc
	s_waitcnt lgkmcnt(0)
	global_store_dwordx4 v[0:1], v[4:7], off
	ds_read_b128 v[0:3], v12 offset:256
	ds_read_b128 v[4:7], v12 offset:384
	v_add_co_u32_e32 v10, vcc, 0x400000, v8
	s_nop 1
	v_addc_co_u32_e32 v11, vcc, 0, v9, vcc
	s_waitcnt lgkmcnt(1)
	global_store_dwordx4 v[10:11], v[0:3], off
	s_nop 1
	v_add_co_u32_e32 v0, vcc, 0x600000, v8
	s_nop 1
	v_addc_co_u32_e32 v1, vcc, 0, v9, vcc
	s_waitcnt lgkmcnt(0)
	global_store_dwordx4 v[0:1], v[4:7], off
	s_andn2_saveexec_b64 s[0:1], s[0:1]
	s_cbranch_execz .LBB1_234
.LBB1_248:
	v_and_b32_e32 v6, 31, v0
	v_bfe_u32 v7, v0, 5, 3
	s_cmp_lt_u32 s8, 0x2000
	s_cselect_b32 s50, s12, s14
	s_cselect_b32 s51, s13, s15
	s_and_b32 s0, s8, 0x1fff
	s_mul_i32 s1, s0, 0x2ee0
	s_add_u32 s50, s50, s1
	s_addc_u32 s51, s51, 0
	s_mov_b32 s52, s50
	s_mov_b32 s53, s51
	s_add_u32 s54, s50, 0x17700
	s_addc_u32 s55, s51, 0
	s_add_u32 s56, s50, 0x2ee00
	s_addc_u32 s57, s51, 0
	s_add_u32 s58, s50, 0x46500
	s_addc_u32 s59, s51, 0
	s_add_u32 s60, s50, 0x5dc00
	s_addc_u32 s61, s51, 0
	s_add_u32 s62, s50, 0x75300
	s_addc_u32 s63, s51, 0
	s_add_u32 s64, s50, 0x8ca00
	s_addc_u32 s65, s51, 0
	s_add_u32 s66, s50, 0xa4100
	s_addc_u32 s67, s51, 0
	v_and_b32_e32 v104, 3, v7
	v_lshl_add_u32 v106, v104, 1, v6
	s_movk_i32 s0, 0x2ee0
	v_mul_lo_u32 v2, v7, s0
	v_lshl_add_u32 v2, v106, 4, v2
	s_movk_i32 s0, 0x110
	v_mul_lo_u32 v3, v7, s0
	v_lshl_add_u32 v107, v106, 3, v3
	v_cmp_le_u32_e64 s[76:77], 32, v106
	v_cmp_gt_u32_e64 s[68:69], 14, v106
	s_not_b64 s[78:79], s[76:77]
	v_mov_b32_e32 v108, 0x0
	v_mov_b32_e32 v109, 0x4300
	v_cndmask_b32_e64 v108, v108, v109, s[76:77]
	v_add_u32_e32 v110, v107, v108
	v_mov_b32_e32 v108, 0x4400
	v_mov_b32_e32 v109, 0x8700
	v_cndmask_b32_e64 v108, v108, v109, s[76:77]
	v_add_u32_e32 v111, v107, v108
	v_mov_b32_e32 v108, 0x8800
	v_mov_b32_e32 v109, 0xffffff00
	v_cndmask_b32_e64 v108, v108, v109, s[76:77]
	v_add_u32_e32 v112, v107, v108
	s_add_u32 s48, s18, 0x100000
	s_addc_u32 s49, s19, 0
	s_lshl_b32 s0, s10, 12
	v_add_u32_e32 v150, 0xfffffe00, v0
	v_lshl_add_u32 v150, v150, 4, s0
	global_load_dwordx4 v[152:155], v150, s[48:49]
	global_load_dwordx4 v[156:159], v150, s[18:19]
	v_mov_b32_e32 v116, 0
	v_mov_b32_e32 v117, 0
	v_mov_b32_e32 v118, 0
	v_mov_b32_e32 v119, 0
	s_mov_b64 s[70:71], exec
	s_mov_b64 exec, s[76:77]
	global_load_dwordx4 v[116:119], v2, s[52:53] offset:-512 nt
	s_mov_b64 exec, s[70:71]
	v_mov_b32_e32 v120, 0
	v_mov_b32_e32 v121, 0
	v_mov_b32_e32 v122, 0
	v_mov_b32_e32 v123, 0
	s_mov_b64 s[70:71], exec
	s_mov_b64 exec, s[76:77]
	global_load_dwordx4 v[120:123], v2, s[54:55] offset:-512 nt
	s_mov_b64 exec, s[70:71]
	v_mov_b32_e32 v124, 0
	v_mov_b32_e32 v125, 0
	v_mov_b32_e32 v126, 0
	v_mov_b32_e32 v127, 0
	s_mov_b64 s[70:71], exec
	s_mov_b64 exec, s[76:77]
	global_load_dwordx4 v[124:127], v2, s[56:57] offset:-512 nt
	s_mov_b64 exec, s[70:71]
	v_mov_b32_e32 v128, 0
	v_mov_b32_e32 v129, 0
	v_mov_b32_e32 v130, 0
	v_mov_b32_e32 v131, 0
	s_mov_b64 s[70:71], exec
	s_mov_b64 exec, s[76:77]
	global_load_dwordx4 v[128:131], v2, s[58:59] offset:-512 nt
	s_mov_b64 exec, s[70:71]
	v_mov_b32_e32 v132, 0
	v_mov_b32_e32 v133, 0
	v_mov_b32_e32 v134, 0
	v_mov_b32_e32 v135, 0
	s_mov_b64 s[70:71], exec
	s_mov_b64 exec, s[76:77]
	global_load_dwordx4 v[132:135], v2, s[60:61] offset:-512 nt
	s_mov_b64 exec, s[70:71]
	v_mov_b32_e32 v136, 0
	v_mov_b32_e32 v137, 0
	v_mov_b32_e32 v138, 0
	v_mov_b32_e32 v139, 0
	s_mov_b64 s[70:71], exec
	s_mov_b64 exec, s[76:77]
	global_load_dwordx4 v[136:139], v2, s[62:63] offset:-512 nt
	s_mov_b64 exec, s[70:71]
	v_mov_b32_e32 v140, 0
	v_mov_b32_e32 v141, 0
	v_mov_b32_e32 v142, 0
	v_mov_b32_e32 v143, 0
	s_mov_b64 s[70:71], exec
	s_mov_b64 exec, s[76:77]
	global_load_dwordx4 v[140:143], v2, s[64:65] offset:-512 nt
	s_mov_b64 exec, s[70:71]
	v_mov_b32_e32 v144, 0
	v_mov_b32_e32 v145, 0
	v_mov_b32_e32 v146, 0
	v_mov_b32_e32 v147, 0
	s_mov_b64 s[70:71], exec
	s_mov_b64 exec, s[76:77]
	global_load_dwordx4 v[144:147], v2, s[66:67] offset:-512 nt
	s_mov_b64 exec, s[70:71]
	global_load_dwordx4 v[8:11], v2, s[52:53] nt
	global_load_dwordx4 v[12:15], v2, s[54:55] nt
	global_load_dwordx4 v[16:19], v2, s[56:57] nt
	global_load_dwordx4 v[20:23], v2, s[58:59] nt
	global_load_dwordx4 v[24:27], v2, s[60:61] nt
	global_load_dwordx4 v[28:31], v2, s[62:63] nt
	global_load_dwordx4 v[32:35], v2, s[64:65] nt
	global_load_dwordx4 v[36:39], v2, s[66:67] nt
	global_load_dwordx4 v[40:43], v2, s[52:53] offset:512 nt
	global_load_dwordx4 v[44:47], v2, s[54:55] offset:512 nt
	global_load_dwordx4 v[48:51], v2, s[56:57] offset:512 nt
	global_load_dwordx4 v[52:55], v2, s[58:59] offset:512 nt
	global_load_dwordx4 v[56:59], v2, s[60:61] offset:512 nt
	global_load_dwordx4 v[60:63], v2, s[62:63] offset:512 nt
	global_load_dwordx4 v[64:67], v2, s[64:65] offset:512 nt
	global_load_dwordx4 v[68:71], v2, s[66:67] offset:512 nt
	global_load_dwordx4 v[72:75], v2, s[52:53] offset:1024 nt
	global_load_dwordx4 v[76:79], v2, s[54:55] offset:1024 nt
	global_load_dwordx4 v[80:83], v2, s[56:57] offset:1024 nt
	global_load_dwordx4 v[84:87], v2, s[58:59] offset:1024 nt
	global_load_dwordx4 v[88:91], v2, s[60:61] offset:1024 nt
	global_load_dwordx4 v[92:95], v2, s[62:63] offset:1024 nt
	global_load_dwordx4 v[96:99], v2, s[64:65] offset:1024 nt
	global_load_dwordx4 v[100:103], v2, s[66:67] offset:1024 nt
	s_waitcnt vmcnt(32)
	v_mov_b32_e32 v151, 1
	v_lshlrev_b32_e32 v160, 2, v152
	v_lshlrev_b32_e32 v161, 2, v153
	v_lshlrev_b32_e32 v162, 2, v154
	v_lshlrev_b32_e32 v163, 2, v155
	global_atomic_add v164, v160, v151, s[20:21] sc0
	global_atomic_add v165, v161, v151, s[20:21] sc0
	global_atomic_add v166, v162, v151, s[20:21] sc0
	global_atomic_add v167, v163, v151, s[20:21] sc0
	s_waitcnt vmcnt(35)
	v_cvt_pk_f16_f32 v4, v116, v117
	v_cvt_pk_f16_f32 v5, v118, v119
	s_mov_b64 s[70:71], exec
	s_mov_b64 exec, s[76:77]
	ds_write_b64 v112, v[4:5]
	s_mov_b64 exec, s[70:71]
	s_waitcnt vmcnt(34)
	v_cvt_pk_f16_f32 v4, v120, v121
	v_cvt_pk_f16_f32 v5, v122, v123
	s_mov_b64 s[70:71], exec
	s_mov_b64 exec, s[76:77]
	ds_write_b64 v112, v[4:5] offset:2176
	s_mov_b64 exec, s[70:71]
	s_waitcnt vmcnt(33)
	v_cvt_pk_f16_f32 v4, v124, v125
	v_cvt_pk_f16_f32 v5, v126, v127
	s_mov_b64 s[70:71], exec
	s_mov_b64 exec, s[76:77]
	ds_write_b64 v112, v[4:5] offset:4352
	s_mov_b64 exec, s[70:71]
	s_waitcnt vmcnt(32)
	v_cvt_pk_f16_f32 v4, v128, v129
	v_cvt_pk_f16_f32 v5, v130, v131
	s_mov_b64 s[70:71], exec
	s_mov_b64 exec, s[76:77]
	ds_write_b64 v112, v[4:5] offset:6528
	s_mov_b64 exec, s[70:71]
	s_waitcnt vmcnt(31)
	v_cvt_pk_f16_f32 v4, v132, v133
	v_cvt_pk_f16_f32 v5, v134, v135
	s_mov_b64 s[70:71], exec
	s_mov_b64 exec, s[76:77]
	ds_write_b64 v112, v[4:5] offset:8704
	s_mov_b64 exec, s[70:71]
	s_waitcnt vmcnt(30)
	v_cvt_pk_f16_f32 v4, v136, v137
	v_cvt_pk_f16_f32 v5, v138, v139
	s_mov_b64 s[70:71], exec
	s_mov_b64 exec, s[76:77]
	ds_write_b64 v112, v[4:5] offset:10880
	s_mov_b64 exec, s[70:71]
	s_waitcnt vmcnt(29)
	v_cvt_pk_f16_f32 v4, v140, v141
	v_cvt_pk_f16_f32 v5, v142, v143
	s_mov_b64 s[70:71], exec
	s_mov_b64 exec, s[76:77]
	ds_write_b64 v112, v[4:5] offset:13056
	s_mov_b64 exec, s[70:71]
	s_waitcnt vmcnt(28)
	v_cvt_pk_f16_f32 v4, v144, v145
	v_cvt_pk_f16_f32 v5, v146, v147
	s_mov_b64 s[70:71], exec
	s_mov_b64 exec, s[76:77]
	ds_write_b64 v112, v[4:5] offset:15232
	s_mov_b64 exec, s[70:71]
	s_waitcnt vmcnt(27)
	v_cvt_pk_f16_f32 v4, v8, v9
	v_cvt_pk_f16_f32 v5, v10, v11
	ds_write_b64 v110, v[4:5]
	global_load_dwordx4 v[8:11], v2, s[52:53] offset:1536 nt
	s_waitcnt vmcnt(27)
	v_cvt_pk_f16_f32 v4, v12, v13
	v_cvt_pk_f16_f32 v5, v14, v15
	ds_write_b64 v110, v[4:5] offset:2176
	global_load_dwordx4 v[12:15], v2, s[54:55] offset:1536 nt
	s_waitcnt vmcnt(27)
	v_cvt_pk_f16_f32 v4, v16, v17
	v_cvt_pk_f16_f32 v5, v18, v19
	ds_write_b64 v110, v[4:5] offset:4352
	global_load_dwordx4 v[16:19], v2, s[56:57] offset:1536 nt
	s_waitcnt vmcnt(27)
	v_cvt_pk_f16_f32 v4, v20, v21
	v_cvt_pk_f16_f32 v5, v22, v23
	ds_write_b64 v110, v[4:5] offset:6528
	global_load_dwordx4 v[20:23], v2, s[58:59] offset:1536 nt
	s_waitcnt vmcnt(27)
	v_cvt_pk_f16_f32 v4, v24, v25
	v_cvt_pk_f16_f32 v5, v26, v27
	ds_write_b64 v110, v[4:5] offset:8704
	global_load_dwordx4 v[24:27], v2, s[60:61] offset:1536 nt
	s_waitcnt vmcnt(27)
	v_cvt_pk_f16_f32 v4, v28, v29
	v_cvt_pk_f16_f32 v5, v30, v31
	ds_write_b64 v110, v[4:5] offset:10880
	global_load_dwordx4 v[28:31], v2, s[62:63] offset:1536 nt
	s_waitcnt vmcnt(27)
	v_cvt_pk_f16_f32 v4, v32, v33
	v_cvt_pk_f16_f32 v5, v34, v35
	ds_write_b64 v110, v[4:5] offset:13056
	global_load_dwordx4 v[32:35], v2, s[64:65] offset:1536 nt
	s_waitcnt vmcnt(27)
	v_cvt_pk_f16_f32 v4, v36, v37
	v_cvt_pk_f16_f32 v5, v38, v39
	ds_write_b64 v110, v[4:5] offset:15232
	global_load_dwordx4 v[36:39], v2, s[66:67] offset:1536 nt
	s_waitcnt vmcnt(0)
	v_cmp_gt_i32_e32 vcc, 64, v164
	v_lshl_add_u32 v148, v152, 6, v164
	v_lshlrev_b32_e32 v148, 2, v148
	s_and_saveexec_b64 s[2:3], vcc
	global_store_dword v148, v156, s[22:23]
	s_xor_b64 exec, exec, s[2:3]
	s_cbranch_execz .Lg1_ld_ok_0
	v_mov_b32_e32 v149, 0x8000
	global_atomic_add v149, v149, v151, s[20:21] sc0
	s_waitcnt vmcnt(0)
	v_lshlrev_b32_e32 v149, 3, v149
	v_mov_b32_e32 v160, v152
	v_mov_b32_e32 v161, v156
	global_store_dwordx2 v149, v[160:161], s[28:29]
.Lg1_ld_ok_0:
	s_mov_b64 exec, -1
	v_cmp_gt_i32_e32 vcc, 64, v165
	v_lshl_add_u32 v148, v153, 6, v165
	v_lshlrev_b32_e32 v148, 2, v148
	s_and_saveexec_b64 s[2:3], vcc
	global_store_dword v148, v157, s[22:23]
	s_xor_b64 exec, exec, s[2:3]
	s_cbranch_execz .Lg1_ld_ok_1
	v_mov_b32_e32 v149, 0x8000
	global_atomic_add v149, v149, v151, s[20:21] sc0
	s_waitcnt vmcnt(0)
	v_lshlrev_b32_e32 v149, 3, v149
	v_mov_b32_e32 v160, v153
	v_mov_b32_e32 v161, v157
	global_store_dwordx2 v149, v[160:161], s[28:29]
.Lg1_ld_ok_1:
	s_mov_b64 exec, -1
	v_cmp_gt_i32_e32 vcc, 64, v166
	v_lshl_add_u32 v148, v154, 6, v166
	v_lshlrev_b32_e32 v148, 2, v148
	s_and_saveexec_b64 s[2:3], vcc
	global_store_dword v148, v158, s[22:23]
	s_xor_b64 exec, exec, s[2:3]
	s_cbranch_execz .Lg1_ld_ok_2
	v_mov_b32_e32 v149, 0x8000
	global_atomic_add v149, v149, v151, s[20:21] sc0
	s_waitcnt vmcnt(0)
	v_lshlrev_b32_e32 v149, 3, v149
	v_mov_b32_e32 v160, v154
	v_mov_b32_e32 v161, v158
	global_store_dwordx2 v149, v[160:161], s[28:29]
.Lg1_ld_ok_2:
	s_mov_b64 exec, -1
	v_cmp_gt_i32_e32 vcc, 64, v167
	v_lshl_add_u32 v148, v155, 6, v167
	v_lshlrev_b32_e32 v148, 2, v148
	s_and_saveexec_b64 s[2:3], vcc
	global_store_dword v148, v159, s[22:23]
	s_xor_b64 exec, exec, s[2:3]
	s_cbranch_execz .Lg1_ld_ok_3
	v_mov_b32_e32 v149, 0x8000
	global_atomic_add v149, v149, v151, s[20:21] sc0
	s_waitcnt vmcnt(0)
	v_lshlrev_b32_e32 v149, 3, v149
	v_mov_b32_e32 v160, v155
	v_mov_b32_e32 v161, v159
	global_store_dwordx2 v149, v[160:161], s[28:29]
.Lg1_ld_ok_3:
	s_mov_b64 exec, -1
	s_waitcnt lgkmcnt(0)
	s_barrier
	s_waitcnt vmcnt(27)
	v_cvt_pk_f16_f32 v4, v40, v41
	v_cvt_pk_f16_f32 v5, v42, v43
	ds_write_b64 v111, v[4:5]
	global_load_dwordx4 v[40:43], v2, s[52:53] offset:2048 nt
	s_waitcnt vmcnt(27)
	v_cvt_pk_f16_f32 v4, v44, v45
	v_cvt_pk_f16_f32 v5, v46, v47
	ds_write_b64 v111, v[4:5] offset:2176
	global_load_dwordx4 v[44:47], v2, s[54:55] offset:2048 nt
	s_waitcnt vmcnt(27)
	v_cvt_pk_f16_f32 v4, v48, v49
	v_cvt_pk_f16_f32 v5, v50, v51
	ds_write_b64 v111, v[4:5] offset:4352
	global_load_dwordx4 v[48:51], v2, s[56:57] offset:2048 nt
	s_waitcnt vmcnt(27)
	v_cvt_pk_f16_f32 v4, v52, v53
	v_cvt_pk_f16_f32 v5, v54, v55
	ds_write_b64 v111, v[4:5] offset:6528
	global_load_dwordx4 v[52:55], v2, s[58:59] offset:2048 nt
	s_waitcnt vmcnt(27)
	v_cvt_pk_f16_f32 v4, v56, v57
	v_cvt_pk_f16_f32 v5, v58, v59
	ds_write_b64 v111, v[4:5] offset:8704
	global_load_dwordx4 v[56:59], v2, s[60:61] offset:2048 nt
	s_waitcnt vmcnt(27)
	v_cvt_pk_f16_f32 v4, v60, v61
	v_cvt_pk_f16_f32 v5, v62, v63
	ds_write_b64 v111, v[4:5] offset:10880
	global_load_dwordx4 v[60:63], v2, s[62:63] offset:2048 nt
	s_waitcnt vmcnt(27)
	v_cvt_pk_f16_f32 v4, v64, v65
	v_cvt_pk_f16_f32 v5, v66, v67
	ds_write_b64 v111, v[4:5] offset:13056
	global_load_dwordx4 v[64:67], v2, s[64:65] offset:2048 nt
	s_waitcnt vmcnt(27)
	v_cvt_pk_f16_f32 v4, v68, v69
	v_cvt_pk_f16_f32 v5, v70, v71
	ds_write_b64 v111, v[4:5] offset:15232
	global_load_dwordx4 v[68:71], v2, s[66:67] offset:2048 nt
	s_waitcnt lgkmcnt(0)
	s_barrier
	s_waitcnt vmcnt(27)
	v_cvt_pk_f16_f32 v4, v72, v73
	v_cvt_pk_f16_f32 v5, v74, v75
	ds_write_b64 v112, v[4:5]
	global_load_dwordx4 v[72:75], v2, s[52:53] offset:2560 nt
	s_waitcnt vmcnt(27)
	v_cvt_pk_f16_f32 v4, v76, v77
	v_cvt_pk_f16_f32 v5, v78, v79
	ds_write_b64 v112, v[4:5] offset:2176
	global_load_dwordx4 v[76:79], v2, s[54:55] offset:2560 nt
	s_waitcnt vmcnt(27)
	v_cvt_pk_f16_f32 v4, v80, v81
	v_cvt_pk_f16_f32 v5, v82, v83
	ds_write_b64 v112, v[4:5] offset:4352
	global_load_dwordx4 v[80:83], v2, s[56:57] offset:2560 nt
	s_waitcnt vmcnt(27)
	v_cvt_pk_f16_f32 v4, v84, v85
	v_cvt_pk_f16_f32 v5, v86, v87
	ds_write_b64 v112, v[4:5] offset:6528
	global_load_dwordx4 v[84:87], v2, s[58:59] offset:2560 nt
	s_waitcnt vmcnt(27)
	v_cvt_pk_f16_f32 v4, v88, v89
	v_cvt_pk_f16_f32 v5, v90, v91
	ds_write_b64 v112, v[4:5] offset:8704
	global_load_dwordx4 v[88:91], v2, s[60:61] offset:2560 nt
	s_waitcnt vmcnt(27)
	v_cvt_pk_f16_f32 v4, v92, v93
	v_cvt_pk_f16_f32 v5, v94, v95
	ds_write_b64 v112, v[4:5] offset:10880
	global_load_dwordx4 v[92:95], v2, s[62:63] offset:2560 nt
	s_waitcnt vmcnt(27)
	v_cvt_pk_f16_f32 v4, v96, v97
	v_cvt_pk_f16_f32 v5, v98, v99
	ds_write_b64 v112, v[4:5] offset:13056
	global_load_dwordx4 v[96:99], v2, s[64:65] offset:2560 nt
	s_waitcnt vmcnt(27)
	v_cvt_pk_f16_f32 v4, v100, v101
	v_cvt_pk_f16_f32 v5, v102, v103
	ds_write_b64 v112, v[4:5] offset:15232
	global_load_dwordx4 v[100:103], v2, s[66:67] offset:2560 nt
	s_waitcnt lgkmcnt(0)
	s_barrier
	s_waitcnt vmcnt(23)
	v_cvt_pk_f16_f32 v4, v8, v9
	v_cvt_pk_f16_f32 v5, v10, v11
	ds_write_b64 v110, v[4:5]
	global_load_dwordx4 v[8:11], v2, s[52:53] offset:3072 nt
	s_waitcnt vmcnt(23)
	v_cvt_pk_f16_f32 v4, v12, v13
	v_cvt_pk_f16_f32 v5, v14, v15
	ds_write_b64 v110, v[4:5] offset:2176
	global_load_dwordx4 v[12:15], v2, s[54:55] offset:3072 nt
	s_waitcnt vmcnt(23)
	v_cvt_pk_f16_f32 v4, v16, v17
	v_cvt_pk_f16_f32 v5, v18, v19
	ds_write_b64 v110, v[4:5] offset:4352
	global_load_dwordx4 v[16:19], v2, s[56:57] offset:3072 nt
	s_waitcnt vmcnt(23)
	v_cvt_pk_f16_f32 v4, v20, v21
	v_cvt_pk_f16_f32 v5, v22, v23
	ds_write_b64 v110, v[4:5] offset:6528
	global_load_dwordx4 v[20:23], v2, s[58:59] offset:3072 nt
	s_waitcnt vmcnt(23)
	v_cvt_pk_f16_f32 v4, v24, v25
	v_cvt_pk_f16_f32 v5, v26, v27
	ds_write_b64 v110, v[4:5] offset:8704
	global_load_dwordx4 v[24:27], v2, s[60:61] offset:3072 nt
	s_waitcnt vmcnt(23)
	v_cvt_pk_f16_f32 v4, v28, v29
	v_cvt_pk_f16_f32 v5, v30, v31
	ds_write_b64 v110, v[4:5] offset:10880
	global_load_dwordx4 v[28:31], v2, s[62:63] offset:3072 nt
	s_waitcnt vmcnt(23)
	v_cvt_pk_f16_f32 v4, v32, v33
	v_cvt_pk_f16_f32 v5, v34, v35
	ds_write_b64 v110, v[4:5] offset:13056
	global_load_dwordx4 v[32:35], v2, s[64:65] offset:3072 nt
	s_waitcnt vmcnt(23)
	v_cvt_pk_f16_f32 v4, v36, v37
	v_cvt_pk_f16_f32 v5, v38, v39
	ds_write_b64 v110, v[4:5] offset:15232
	global_load_dwordx4 v[36:39], v2, s[66:67] offset:3072 nt
	s_waitcnt lgkmcnt(0)
	s_barrier
	s_waitcnt vmcnt(23)
	v_cvt_pk_f16_f32 v4, v40, v41
	v_cvt_pk_f16_f32 v5, v42, v43
	ds_write_b64 v111, v[4:5]
	global_load_dwordx4 v[40:43], v2, s[52:53] offset:3584 nt
	s_waitcnt vmcnt(23)
	v_cvt_pk_f16_f32 v4, v44, v45
	v_cvt_pk_f16_f32 v5, v46, v47
	ds_write_b64 v111, v[4:5] offset:2176
	global_load_dwordx4 v[44:47], v2, s[54:55] offset:3584 nt
	s_waitcnt vmcnt(23)
	v_cvt_pk_f16_f32 v4, v48, v49
	v_cvt_pk_f16_f32 v5, v50, v51
	ds_write_b64 v111, v[4:5] offset:4352
	global_load_dwordx4 v[48:51], v2, s[56:57] offset:3584 nt
	s_waitcnt vmcnt(23)
	v_cvt_pk_f16_f32 v4, v52, v53
	v_cvt_pk_f16_f32 v5, v54, v55
	ds_write_b64 v111, v[4:5] offset:6528
	global_load_dwordx4 v[52:55], v2, s[58:59] offset:3584 nt
	s_waitcnt vmcnt(23)
	v_cvt_pk_f16_f32 v4, v56, v57
	v_cvt_pk_f16_f32 v5, v58, v59
	ds_write_b64 v111, v[4:5] offset:8704
	global_load_dwordx4 v[56:59], v2, s[60:61] offset:3584 nt
	s_waitcnt vmcnt(23)
	v_cvt_pk_f16_f32 v4, v60, v61
	v_cvt_pk_f16_f32 v5, v62, v63
	ds_write_b64 v111, v[4:5] offset:10880
	global_load_dwordx4 v[60:63], v2, s[62:63] offset:3584 nt
	s_waitcnt vmcnt(23)
	v_cvt_pk_f16_f32 v4, v64, v65
	v_cvt_pk_f16_f32 v5, v66, v67
	ds_write_b64 v111, v[4:5] offset:13056
	global_load_dwordx4 v[64:67], v2, s[64:65] offset:3584 nt
	s_waitcnt vmcnt(23)
	v_cvt_pk_f16_f32 v4, v68, v69
	v_cvt_pk_f16_f32 v5, v70, v71
	ds_write_b64 v111, v[4:5] offset:15232
	global_load_dwordx4 v[68:71], v2, s[66:67] offset:3584 nt
	s_waitcnt lgkmcnt(0)
	s_barrier
	s_waitcnt vmcnt(23)
	v_cvt_pk_f16_f32 v4, v72, v73
	v_cvt_pk_f16_f32 v5, v74, v75
	ds_write_b64 v112, v[4:5]
	v_add_u32_e32 v2, 0x1000, v2
	global_load_dwordx4 v[72:75], v2, s[52:53] nt
	s_waitcnt vmcnt(23)
	v_cvt_pk_f16_f32 v4, v76, v77
	v_cvt_pk_f16_f32 v5, v78, v79
	ds_write_b64 v112, v[4:5] offset:2176
	global_load_dwordx4 v[76:79], v2, s[54:55] nt
	s_waitcnt vmcnt(23)
	v_cvt_pk_f16_f32 v4, v80, v81
	v_cvt_pk_f16_f32 v5, v82, v83
	ds_write_b64 v112, v[4:5] offset:4352
	global_load_dwordx4 v[80:83], v2, s[56:57] nt
	s_waitcnt vmcnt(23)
	v_cvt_pk_f16_f32 v4, v84, v85
	v_cvt_pk_f16_f32 v5, v86, v87
	ds_write_b64 v112, v[4:5] offset:6528
	global_load_dwordx4 v[84:87], v2, s[58:59] nt
	s_waitcnt vmcnt(23)
	v_cvt_pk_f16_f32 v4, v88, v89
	v_cvt_pk_f16_f32 v5, v90, v91
	ds_write_b64 v112, v[4:5] offset:8704
	global_load_dwordx4 v[88:91], v2, s[60:61] nt
	s_waitcnt vmcnt(23)
	v_cvt_pk_f16_f32 v4, v92, v93
	v_cvt_pk_f16_f32 v5, v94, v95
	ds_write_b64 v112, v[4:5] offset:10880
	global_load_dwordx4 v[92:95], v2, s[62:63] nt
	s_waitcnt vmcnt(23)
	v_cvt_pk_f16_f32 v4, v96, v97
	v_cvt_pk_f16_f32 v5, v98, v99
	ds_write_b64 v112, v[4:5] offset:13056
	global_load_dwordx4 v[96:99], v2, s[64:65] nt
	s_waitcnt vmcnt(23)
	v_cvt_pk_f16_f32 v4, v100, v101
	v_cvt_pk_f16_f32 v5, v102, v103
	ds_write_b64 v112, v[4:5] offset:15232
	global_load_dwordx4 v[100:103], v2, s[66:67] nt
	s_waitcnt lgkmcnt(0)
	s_barrier
	s_waitcnt vmcnt(23)
	v_cvt_pk_f16_f32 v4, v8, v9
	v_cvt_pk_f16_f32 v5, v10, v11
	ds_write_b64 v110, v[4:5]
	global_load_dwordx4 v[8:11], v2, s[52:53] offset:512 nt
	s_waitcnt vmcnt(23)
	v_cvt_pk_f16_f32 v4, v12, v13
	v_cvt_pk_f16_f32 v5, v14, v15
	ds_write_b64 v110, v[4:5] offset:2176
	global_load_dwordx4 v[12:15], v2, s[54:55] offset:512 nt
	s_waitcnt vmcnt(23)
	v_cvt_pk_f16_f32 v4, v16, v17
	v_cvt_pk_f16_f32 v5, v18, v19
	ds_write_b64 v110, v[4:5] offset:4352
	global_load_dwordx4 v[16:19], v2, s[56:57] offset:512 nt
	s_waitcnt vmcnt(23)
	v_cvt_pk_f16_f32 v4, v20, v21
	v_cvt_pk_f16_f32 v5, v22, v23
	ds_write_b64 v110, v[4:5] offset:6528
	global_load_dwordx4 v[20:23], v2, s[58:59] offset:512 nt
	s_waitcnt vmcnt(23)
	v_cvt_pk_f16_f32 v4, v24, v25
	v_cvt_pk_f16_f32 v5, v26, v27
	ds_write_b64 v110, v[4:5] offset:8704
	global_load_dwordx4 v[24:27], v2, s[60:61] offset:512 nt
	s_waitcnt vmcnt(23)
	v_cvt_pk_f16_f32 v4, v28, v29
	v_cvt_pk_f16_f32 v5, v30, v31
	ds_write_b64 v110, v[4:5] offset:10880
	global_load_dwordx4 v[28:31], v2, s[62:63] offset:512 nt
	s_waitcnt vmcnt(23)
	v_cvt_pk_f16_f32 v4, v32, v33
	v_cvt_pk_f16_f32 v5, v34, v35
	ds_write_b64 v110, v[4:5] offset:13056
	global_load_dwordx4 v[32:35], v2, s[64:65] offset:512 nt
	s_waitcnt vmcnt(23)
	v_cvt_pk_f16_f32 v4, v36, v37
	v_cvt_pk_f16_f32 v5, v38, v39
	ds_write_b64 v110, v[4:5] offset:15232
	global_load_dwordx4 v[36:39], v2, s[66:67] offset:512 nt
	s_waitcnt lgkmcnt(0)
	s_barrier
	s_waitcnt vmcnt(23)
	v_cvt_pk_f16_f32 v4, v40, v41
	v_cvt_pk_f16_f32 v5, v42, v43
	ds_write_b64 v111, v[4:5]
	global_load_dwordx4 v[40:43], v2, s[52:53] offset:1024 nt
	s_waitcnt vmcnt(23)
	v_cvt_pk_f16_f32 v4, v44, v45
	v_cvt_pk_f16_f32 v5, v46, v47
	ds_write_b64 v111, v[4:5] offset:2176
	global_load_dwordx4 v[44:47], v2, s[54:55] offset:1024 nt
	s_waitcnt vmcnt(23)
	v_cvt_pk_f16_f32 v4, v48, v49
	v_cvt_pk_f16_f32 v5, v50, v51
	ds_write_b64 v111, v[4:5] offset:4352
	global_load_dwordx4 v[48:51], v2, s[56:57] offset:1024 nt
	s_waitcnt vmcnt(23)
	v_cvt_pk_f16_f32 v4, v52, v53
	v_cvt_pk_f16_f32 v5, v54, v55
	ds_write_b64 v111, v[4:5] offset:6528
	global_load_dwordx4 v[52:55], v2, s[58:59] offset:1024 nt
	s_waitcnt vmcnt(23)
	v_cvt_pk_f16_f32 v4, v56, v57
	v_cvt_pk_f16_f32 v5, v58, v59
	ds_write_b64 v111, v[4:5] offset:8704
	global_load_dwordx4 v[56:59], v2, s[60:61] offset:1024 nt
	s_waitcnt vmcnt(23)
	v_cvt_pk_f16_f32 v4, v60, v61
	v_cvt_pk_f16_f32 v5, v62, v63
	ds_write_b64 v111, v[4:5] offset:10880
	global_load_dwordx4 v[60:63], v2, s[62:63] offset:1024 nt
	s_waitcnt vmcnt(23)
	v_cvt_pk_f16_f32 v4, v64, v65
	v_cvt_pk_f16_f32 v5, v66, v67
	ds_write_b64 v111, v[4:5] offset:13056
	global_load_dwordx4 v[64:67], v2, s[64:65] offset:1024 nt
	s_waitcnt vmcnt(23)
	v_cvt_pk_f16_f32 v4, v68, v69
	v_cvt_pk_f16_f32 v5, v70, v71
	ds_write_b64 v111, v[4:5] offset:15232
	global_load_dwordx4 v[68:71], v2, s[66:67] offset:1024 nt
	s_waitcnt lgkmcnt(0)
	s_barrier
	s_waitcnt vmcnt(23)
	v_cvt_pk_f16_f32 v4, v72, v73
	v_cvt_pk_f16_f32 v5, v74, v75
	ds_write_b64 v112, v[4:5]
	global_load_dwordx4 v[72:75], v2, s[52:53] offset:1536 nt
	s_waitcnt vmcnt(23)
	v_cvt_pk_f16_f32 v4, v76, v77
	v_cvt_pk_f16_f32 v5, v78, v79
	ds_write_b64 v112, v[4:5] offset:2176
	global_load_dwordx4 v[76:79], v2, s[54:55] offset:1536 nt
	s_waitcnt vmcnt(23)
	v_cvt_pk_f16_f32 v4, v80, v81
	v_cvt_pk_f16_f32 v5, v82, v83
	ds_write_b64 v112, v[4:5] offset:4352
	global_load_dwordx4 v[80:83], v2, s[56:57] offset:1536 nt
	s_waitcnt vmcnt(23)
	v_cvt_pk_f16_f32 v4, v84, v85
	v_cvt_pk_f16_f32 v5, v86, v87
	ds_write_b64 v112, v[4:5] offset:6528
	global_load_dwordx4 v[84:87], v2, s[58:59] offset:1536 nt
	s_waitcnt vmcnt(23)
	v_cvt_pk_f16_f32 v4, v88, v89
	v_cvt_pk_f16_f32 v5, v90, v91
	ds_write_b64 v112, v[4:5] offset:8704
	global_load_dwordx4 v[88:91], v2, s[60:61] offset:1536 nt
	s_waitcnt vmcnt(23)
	v_cvt_pk_f16_f32 v4, v92, v93
	v_cvt_pk_f16_f32 v5, v94, v95
	ds_write_b64 v112, v[4:5] offset:10880
	global_load_dwordx4 v[92:95], v2, s[62:63] offset:1536 nt
	s_waitcnt vmcnt(23)
	v_cvt_pk_f16_f32 v4, v96, v97
	v_cvt_pk_f16_f32 v5, v98, v99
	ds_write_b64 v112, v[4:5] offset:13056
	global_load_dwordx4 v[96:99], v2, s[64:65] offset:1536 nt
	s_waitcnt vmcnt(23)
	v_cvt_pk_f16_f32 v4, v100, v101
	v_cvt_pk_f16_f32 v5, v102, v103
	ds_write_b64 v112, v[4:5] offset:15232
	global_load_dwordx4 v[100:103], v2, s[66:67] offset:1536 nt
	s_waitcnt lgkmcnt(0)
	s_barrier
	s_waitcnt vmcnt(23)
	v_cvt_pk_f16_f32 v4, v8, v9
	v_cvt_pk_f16_f32 v5, v10, v11
	ds_write_b64 v110, v[4:5]
	global_load_dwordx4 v[8:11], v2, s[52:53] offset:2048 nt
	s_waitcnt vmcnt(23)
	v_cvt_pk_f16_f32 v4, v12, v13
	v_cvt_pk_f16_f32 v5, v14, v15
	ds_write_b64 v110, v[4:5] offset:2176
	global_load_dwordx4 v[12:15], v2, s[54:55] offset:2048 nt
	s_waitcnt vmcnt(23)
	v_cvt_pk_f16_f32 v4, v16, v17
	v_cvt_pk_f16_f32 v5, v18, v19
	ds_write_b64 v110, v[4:5] offset:4352
	global_load_dwordx4 v[16:19], v2, s[56:57] offset:2048 nt
	s_waitcnt vmcnt(23)
	v_cvt_pk_f16_f32 v4, v20, v21
	v_cvt_pk_f16_f32 v5, v22, v23
	ds_write_b64 v110, v[4:5] offset:6528
	global_load_dwordx4 v[20:23], v2, s[58:59] offset:2048 nt
	s_waitcnt vmcnt(23)
	v_cvt_pk_f16_f32 v4, v24, v25
	v_cvt_pk_f16_f32 v5, v26, v27
	ds_write_b64 v110, v[4:5] offset:8704
	global_load_dwordx4 v[24:27], v2, s[60:61] offset:2048 nt
	s_waitcnt vmcnt(23)
	v_cvt_pk_f16_f32 v4, v28, v29
	v_cvt_pk_f16_f32 v5, v30, v31
	ds_write_b64 v110, v[4:5] offset:10880
	global_load_dwordx4 v[28:31], v2, s[62:63] offset:2048 nt
	s_waitcnt vmcnt(23)
	v_cvt_pk_f16_f32 v4, v32, v33
	v_cvt_pk_f16_f32 v5, v34, v35
	ds_write_b64 v110, v[4:5] offset:13056
	global_load_dwordx4 v[32:35], v2, s[64:65] offset:2048 nt
	s_waitcnt vmcnt(23)
	v_cvt_pk_f16_f32 v4, v36, v37
	v_cvt_pk_f16_f32 v5, v38, v39
	ds_write_b64 v110, v[4:5] offset:15232
	global_load_dwordx4 v[36:39], v2, s[66:67] offset:2048 nt
	s_waitcnt lgkmcnt(0)
	s_barrier
	s_waitcnt vmcnt(23)
	v_cvt_pk_f16_f32 v4, v40, v41
	v_cvt_pk_f16_f32 v5, v42, v43
	ds_write_b64 v111, v[4:5]
	global_load_dwordx4 v[40:43], v2, s[52:53] offset:2560 nt
	s_waitcnt vmcnt(23)
	v_cvt_pk_f16_f32 v4, v44, v45
	v_cvt_pk_f16_f32 v5, v46, v47
	ds_write_b64 v111, v[4:5] offset:2176
	global_load_dwordx4 v[44:47], v2, s[54:55] offset:2560 nt
	s_waitcnt vmcnt(23)
	v_cvt_pk_f16_f32 v4, v48, v49
	v_cvt_pk_f16_f32 v5, v50, v51
	ds_write_b64 v111, v[4:5] offset:4352
	global_load_dwordx4 v[48:51], v2, s[56:57] offset:2560 nt
	s_waitcnt vmcnt(23)
	v_cvt_pk_f16_f32 v4, v52, v53
	v_cvt_pk_f16_f32 v5, v54, v55
	ds_write_b64 v111, v[4:5] offset:6528
	global_load_dwordx4 v[52:55], v2, s[58:59] offset:2560 nt
	s_waitcnt vmcnt(23)
	v_cvt_pk_f16_f32 v4, v56, v57
	v_cvt_pk_f16_f32 v5, v58, v59
	ds_write_b64 v111, v[4:5] offset:8704
	global_load_dwordx4 v[56:59], v2, s[60:61] offset:2560 nt
	s_waitcnt vmcnt(23)
	v_cvt_pk_f16_f32 v4, v60, v61
	v_cvt_pk_f16_f32 v5, v62, v63
	ds_write_b64 v111, v[4:5] offset:10880
	global_load_dwordx4 v[60:63], v2, s[62:63] offset:2560 nt
	s_waitcnt vmcnt(23)
	v_cvt_pk_f16_f32 v4, v64, v65
	v_cvt_pk_f16_f32 v5, v66, v67
	ds_write_b64 v111, v[4:5] offset:13056
	global_load_dwordx4 v[64:67], v2, s[64:65] offset:2560 nt
	s_waitcnt vmcnt(23)
	v_cvt_pk_f16_f32 v4, v68, v69
	v_cvt_pk_f16_f32 v5, v70, v71
	ds_write_b64 v111, v[4:5] offset:15232
	global_load_dwordx4 v[68:71], v2, s[66:67] offset:2560 nt
	s_waitcnt lgkmcnt(0)
	s_barrier
	s_waitcnt vmcnt(23)
	v_cvt_pk_f16_f32 v4, v72, v73
	v_cvt_pk_f16_f32 v5, v74, v75
	ds_write_b64 v112, v[4:5]
	global_load_dwordx4 v[72:75], v2, s[52:53] offset:3072 nt
	s_waitcnt vmcnt(23)
	v_cvt_pk_f16_f32 v4, v76, v77
	v_cvt_pk_f16_f32 v5, v78, v79
	ds_write_b64 v112, v[4:5] offset:2176
	global_load_dwordx4 v[76:79], v2, s[54:55] offset:3072 nt
	s_waitcnt vmcnt(23)
	v_cvt_pk_f16_f32 v4, v80, v81
	v_cvt_pk_f16_f32 v5, v82, v83
	ds_write_b64 v112, v[4:5] offset:4352
	global_load_dwordx4 v[80:83], v2, s[56:57] offset:3072 nt
	s_waitcnt vmcnt(23)
	v_cvt_pk_f16_f32 v4, v84, v85
	v_cvt_pk_f16_f32 v5, v86, v87
	ds_write_b64 v112, v[4:5] offset:6528
	global_load_dwordx4 v[84:87], v2, s[58:59] offset:3072 nt
	s_waitcnt vmcnt(23)
	v_cvt_pk_f16_f32 v4, v88, v89
	v_cvt_pk_f16_f32 v5, v90, v91
	ds_write_b64 v112, v[4:5] offset:8704
	global_load_dwordx4 v[88:91], v2, s[60:61] offset:3072 nt
	s_waitcnt vmcnt(23)
	v_cvt_pk_f16_f32 v4, v92, v93
	v_cvt_pk_f16_f32 v5, v94, v95
	ds_write_b64 v112, v[4:5] offset:10880
	global_load_dwordx4 v[92:95], v2, s[62:63] offset:3072 nt
	s_waitcnt vmcnt(23)
	v_cvt_pk_f16_f32 v4, v96, v97
	v_cvt_pk_f16_f32 v5, v98, v99
	ds_write_b64 v112, v[4:5] offset:13056
	global_load_dwordx4 v[96:99], v2, s[64:65] offset:3072 nt
	s_waitcnt vmcnt(23)
	v_cvt_pk_f16_f32 v4, v100, v101
	v_cvt_pk_f16_f32 v5, v102, v103
	ds_write_b64 v112, v[4:5] offset:15232
	global_load_dwordx4 v[100:103], v2, s[66:67] offset:3072 nt
	s_waitcnt lgkmcnt(0)
	s_barrier
	s_waitcnt vmcnt(23)
	v_cvt_pk_f16_f32 v4, v8, v9
	v_cvt_pk_f16_f32 v5, v10, v11
	ds_write_b64 v110, v[4:5]
	global_load_dwordx4 v[8:11], v2, s[52:53] offset:3584 nt
	s_waitcnt vmcnt(23)
	v_cvt_pk_f16_f32 v4, v12, v13
	v_cvt_pk_f16_f32 v5, v14, v15
	ds_write_b64 v110, v[4:5] offset:2176
	global_load_dwordx4 v[12:15], v2, s[54:55] offset:3584 nt
	s_waitcnt vmcnt(23)
	v_cvt_pk_f16_f32 v4, v16, v17
	v_cvt_pk_f16_f32 v5, v18, v19
	ds_write_b64 v110, v[4:5] offset:4352
	global_load_dwordx4 v[16:19], v2, s[56:57] offset:3584 nt
	s_waitcnt vmcnt(23)
	v_cvt_pk_f16_f32 v4, v20, v21
	v_cvt_pk_f16_f32 v5, v22, v23
	ds_write_b64 v110, v[4:5] offset:6528
	global_load_dwordx4 v[20:23], v2, s[58:59] offset:3584 nt
	s_waitcnt vmcnt(23)
	v_cvt_pk_f16_f32 v4, v24, v25
	v_cvt_pk_f16_f32 v5, v26, v27
	ds_write_b64 v110, v[4:5] offset:8704
	global_load_dwordx4 v[24:27], v2, s[60:61] offset:3584 nt
	s_waitcnt vmcnt(23)
	v_cvt_pk_f16_f32 v4, v28, v29
	v_cvt_pk_f16_f32 v5, v30, v31
	ds_write_b64 v110, v[4:5] offset:10880
	global_load_dwordx4 v[28:31], v2, s[62:63] offset:3584 nt
	s_waitcnt vmcnt(23)
	v_cvt_pk_f16_f32 v4, v32, v33
	v_cvt_pk_f16_f32 v5, v34, v35
	ds_write_b64 v110, v[4:5] offset:13056
	global_load_dwordx4 v[32:35], v2, s[64:65] offset:3584 nt
	s_waitcnt vmcnt(23)
	v_cvt_pk_f16_f32 v4, v36, v37
	v_cvt_pk_f16_f32 v5, v38, v39
	ds_write_b64 v110, v[4:5] offset:15232
	global_load_dwordx4 v[36:39], v2, s[66:67] offset:3584 nt
	s_waitcnt lgkmcnt(0)
	s_barrier
	s_waitcnt vmcnt(23)
	v_cvt_pk_f16_f32 v4, v40, v41
	v_cvt_pk_f16_f32 v5, v42, v43
	ds_write_b64 v111, v[4:5]
	v_add_u32_e32 v2, 0x1000, v2
	global_load_dwordx4 v[40:43], v2, s[52:53] nt
	s_waitcnt vmcnt(23)
	v_cvt_pk_f16_f32 v4, v44, v45
	v_cvt_pk_f16_f32 v5, v46, v47
	ds_write_b64 v111, v[4:5] offset:2176
	global_load_dwordx4 v[44:47], v2, s[54:55] nt
	s_waitcnt vmcnt(23)
	v_cvt_pk_f16_f32 v4, v48, v49
	v_cvt_pk_f16_f32 v5, v50, v51
	ds_write_b64 v111, v[4:5] offset:4352
	global_load_dwordx4 v[48:51], v2, s[56:57] nt
	s_waitcnt vmcnt(23)
	v_cvt_pk_f16_f32 v4, v52, v53
	v_cvt_pk_f16_f32 v5, v54, v55
	ds_write_b64 v111, v[4:5] offset:6528
	global_load_dwordx4 v[52:55], v2, s[58:59] nt
	s_waitcnt vmcnt(23)
	v_cvt_pk_f16_f32 v4, v56, v57
	v_cvt_pk_f16_f32 v5, v58, v59
	ds_write_b64 v111, v[4:5] offset:8704
	global_load_dwordx4 v[56:59], v2, s[60:61] nt
	s_waitcnt vmcnt(23)
	v_cvt_pk_f16_f32 v4, v60, v61
	v_cvt_pk_f16_f32 v5, v62, v63
	ds_write_b64 v111, v[4:5] offset:10880
	global_load_dwordx4 v[60:63], v2, s[62:63] nt
	s_waitcnt vmcnt(23)
	v_cvt_pk_f16_f32 v4, v64, v65
	v_cvt_pk_f16_f32 v5, v66, v67
	ds_write_b64 v111, v[4:5] offset:13056
	global_load_dwordx4 v[64:67], v2, s[64:65] nt
	s_waitcnt vmcnt(23)
	v_cvt_pk_f16_f32 v4, v68, v69
	v_cvt_pk_f16_f32 v5, v70, v71
	ds_write_b64 v111, v[4:5] offset:15232
	global_load_dwordx4 v[68:71], v2, s[66:67] nt
	s_waitcnt lgkmcnt(0)
	s_barrier
	s_waitcnt vmcnt(23)
	v_cvt_pk_f16_f32 v4, v72, v73
	v_cvt_pk_f16_f32 v5, v74, v75
	ds_write_b64 v112, v[4:5]
	global_load_dwordx4 v[72:75], v2, s[52:53] offset:512 nt
	s_waitcnt vmcnt(23)
	v_cvt_pk_f16_f32 v4, v76, v77
	v_cvt_pk_f16_f32 v5, v78, v79
	ds_write_b64 v112, v[4:5] offset:2176
	global_load_dwordx4 v[76:79], v2, s[54:55] offset:512 nt
	s_waitcnt vmcnt(23)
	v_cvt_pk_f16_f32 v4, v80, v81
	v_cvt_pk_f16_f32 v5, v82, v83
	ds_write_b64 v112, v[4:5] offset:4352
	global_load_dwordx4 v[80:83], v2, s[56:57] offset:512 nt
	s_waitcnt vmcnt(23)
	v_cvt_pk_f16_f32 v4, v84, v85
	v_cvt_pk_f16_f32 v5, v86, v87
	ds_write_b64 v112, v[4:5] offset:6528
	global_load_dwordx4 v[84:87], v2, s[58:59] offset:512 nt
	s_waitcnt vmcnt(23)
	v_cvt_pk_f16_f32 v4, v88, v89
	v_cvt_pk_f16_f32 v5, v90, v91
	ds_write_b64 v112, v[4:5] offset:8704
	global_load_dwordx4 v[88:91], v2, s[60:61] offset:512 nt
	s_waitcnt vmcnt(23)
	v_cvt_pk_f16_f32 v4, v92, v93
	v_cvt_pk_f16_f32 v5, v94, v95
	ds_write_b64 v112, v[4:5] offset:10880
	global_load_dwordx4 v[92:95], v2, s[62:63] offset:512 nt
	s_waitcnt vmcnt(23)
	v_cvt_pk_f16_f32 v4, v96, v97
	v_cvt_pk_f16_f32 v5, v98, v99
	ds_write_b64 v112, v[4:5] offset:13056
	global_load_dwordx4 v[96:99], v2, s[64:65] offset:512 nt
	s_waitcnt vmcnt(23)
	v_cvt_pk_f16_f32 v4, v100, v101
	v_cvt_pk_f16_f32 v5, v102, v103
	ds_write_b64 v112, v[4:5] offset:15232
	global_load_dwordx4 v[100:103], v2, s[66:67] offset:512 nt
	s_waitcnt lgkmcnt(0)
	s_barrier
	s_waitcnt vmcnt(23)
	v_cvt_pk_f16_f32 v4, v8, v9
	v_cvt_pk_f16_f32 v5, v10, v11
	ds_write_b64 v110, v[4:5]
	global_load_dwordx4 v[8:11], v2, s[52:53] offset:1024 nt
	s_waitcnt vmcnt(23)
	v_cvt_pk_f16_f32 v4, v12, v13
	v_cvt_pk_f16_f32 v5, v14, v15
	ds_write_b64 v110, v[4:5] offset:2176
	global_load_dwordx4 v[12:15], v2, s[54:55] offset:1024 nt
	s_waitcnt vmcnt(23)
	v_cvt_pk_f16_f32 v4, v16, v17
	v_cvt_pk_f16_f32 v5, v18, v19
	ds_write_b64 v110, v[4:5] offset:4352
	global_load_dwordx4 v[16:19], v2, s[56:57] offset:1024 nt
	s_waitcnt vmcnt(23)
	v_cvt_pk_f16_f32 v4, v20, v21
	v_cvt_pk_f16_f32 v5, v22, v23
	ds_write_b64 v110, v[4:5] offset:6528
	global_load_dwordx4 v[20:23], v2, s[58:59] offset:1024 nt
	s_waitcnt vmcnt(23)
	v_cvt_pk_f16_f32 v4, v24, v25
	v_cvt_pk_f16_f32 v5, v26, v27
	ds_write_b64 v110, v[4:5] offset:8704
	global_load_dwordx4 v[24:27], v2, s[60:61] offset:1024 nt
	s_waitcnt vmcnt(23)
	v_cvt_pk_f16_f32 v4, v28, v29
	v_cvt_pk_f16_f32 v5, v30, v31
	ds_write_b64 v110, v[4:5] offset:10880
	global_load_dwordx4 v[28:31], v2, s[62:63] offset:1024 nt
	s_waitcnt vmcnt(23)
	v_cvt_pk_f16_f32 v4, v32, v33
	v_cvt_pk_f16_f32 v5, v34, v35
	ds_write_b64 v110, v[4:5] offset:13056
	global_load_dwordx4 v[32:35], v2, s[64:65] offset:1024 nt
	s_waitcnt vmcnt(23)
	v_cvt_pk_f16_f32 v4, v36, v37
	v_cvt_pk_f16_f32 v5, v38, v39
	ds_write_b64 v110, v[4:5] offset:15232
	global_load_dwordx4 v[36:39], v2, s[66:67] offset:1024 nt
	s_waitcnt lgkmcnt(0)
	s_barrier
	s_waitcnt vmcnt(23)
	v_cvt_pk_f16_f32 v4, v40, v41
	v_cvt_pk_f16_f32 v5, v42, v43
	ds_write_b64 v111, v[4:5]
	global_load_dwordx4 v[40:43], v2, s[52:53] offset:1536 nt
	s_waitcnt vmcnt(23)
	v_cvt_pk_f16_f32 v4, v44, v45
	v_cvt_pk_f16_f32 v5, v46, v47
	ds_write_b64 v111, v[4:5] offset:2176
	global_load_dwordx4 v[44:47], v2, s[54:55] offset:1536 nt
	s_waitcnt vmcnt(23)
	v_cvt_pk_f16_f32 v4, v48, v49
	v_cvt_pk_f16_f32 v5, v50, v51
	ds_write_b64 v111, v[4:5] offset:4352
	global_load_dwordx4 v[48:51], v2, s[56:57] offset:1536 nt
	s_waitcnt vmcnt(23)
	v_cvt_pk_f16_f32 v4, v52, v53
	v_cvt_pk_f16_f32 v5, v54, v55
	ds_write_b64 v111, v[4:5] offset:6528
	global_load_dwordx4 v[52:55], v2, s[58:59] offset:1536 nt
	s_waitcnt vmcnt(23)
	v_cvt_pk_f16_f32 v4, v56, v57
	v_cvt_pk_f16_f32 v5, v58, v59
	ds_write_b64 v111, v[4:5] offset:8704
	global_load_dwordx4 v[56:59], v2, s[60:61] offset:1536 nt
	s_waitcnt vmcnt(23)
	v_cvt_pk_f16_f32 v4, v60, v61
	v_cvt_pk_f16_f32 v5, v62, v63
	ds_write_b64 v111, v[4:5] offset:10880
	global_load_dwordx4 v[60:63], v2, s[62:63] offset:1536 nt
	s_waitcnt vmcnt(23)
	v_cvt_pk_f16_f32 v4, v64, v65
	v_cvt_pk_f16_f32 v5, v66, v67
	ds_write_b64 v111, v[4:5] offset:13056
	global_load_dwordx4 v[64:67], v2, s[64:65] offset:1536 nt
	s_waitcnt vmcnt(23)
	v_cvt_pk_f16_f32 v4, v68, v69
	v_cvt_pk_f16_f32 v5, v70, v71
	ds_write_b64 v111, v[4:5] offset:15232
	global_load_dwordx4 v[68:71], v2, s[66:67] offset:1536 nt
	s_waitcnt lgkmcnt(0)
	s_barrier
	s_waitcnt vmcnt(23)
	v_cvt_pk_f16_f32 v4, v72, v73
	v_cvt_pk_f16_f32 v5, v74, v75
	ds_write_b64 v112, v[4:5]
	global_load_dwordx4 v[72:75], v2, s[52:53] offset:2048 nt
	s_waitcnt vmcnt(23)
	v_cvt_pk_f16_f32 v4, v76, v77
	v_cvt_pk_f16_f32 v5, v78, v79
	ds_write_b64 v112, v[4:5] offset:2176
	global_load_dwordx4 v[76:79], v2, s[54:55] offset:2048 nt
	s_waitcnt vmcnt(23)
	v_cvt_pk_f16_f32 v4, v80, v81
	v_cvt_pk_f16_f32 v5, v82, v83
	ds_write_b64 v112, v[4:5] offset:4352
	global_load_dwordx4 v[80:83], v2, s[56:57] offset:2048 nt
	s_waitcnt vmcnt(23)
	v_cvt_pk_f16_f32 v4, v84, v85
	v_cvt_pk_f16_f32 v5, v86, v87
	ds_write_b64 v112, v[4:5] offset:6528
	global_load_dwordx4 v[84:87], v2, s[58:59] offset:2048 nt
	s_waitcnt vmcnt(23)
	v_cvt_pk_f16_f32 v4, v88, v89
	v_cvt_pk_f16_f32 v5, v90, v91
	ds_write_b64 v112, v[4:5] offset:8704
	global_load_dwordx4 v[88:91], v2, s[60:61] offset:2048 nt
	s_waitcnt vmcnt(23)
	v_cvt_pk_f16_f32 v4, v92, v93
	v_cvt_pk_f16_f32 v5, v94, v95
	ds_write_b64 v112, v[4:5] offset:10880
	global_load_dwordx4 v[92:95], v2, s[62:63] offset:2048 nt
	s_waitcnt vmcnt(23)
	v_cvt_pk_f16_f32 v4, v96, v97
	v_cvt_pk_f16_f32 v5, v98, v99
	ds_write_b64 v112, v[4:5] offset:13056
	global_load_dwordx4 v[96:99], v2, s[64:65] offset:2048 nt
	s_waitcnt vmcnt(23)
	v_cvt_pk_f16_f32 v4, v100, v101
	v_cvt_pk_f16_f32 v5, v102, v103
	ds_write_b64 v112, v[4:5] offset:15232
	global_load_dwordx4 v[100:103], v2, s[66:67] offset:2048 nt
	s_waitcnt lgkmcnt(0)
	s_barrier
	s_waitcnt vmcnt(23)
	v_cvt_pk_f16_f32 v4, v8, v9
	v_cvt_pk_f16_f32 v5, v10, v11
	ds_write_b64 v110, v[4:5]
	global_load_dwordx4 v[8:11], v2, s[52:53] offset:2560 nt
	s_waitcnt vmcnt(23)
	v_cvt_pk_f16_f32 v4, v12, v13
	v_cvt_pk_f16_f32 v5, v14, v15
	ds_write_b64 v110, v[4:5] offset:2176
	global_load_dwordx4 v[12:15], v2, s[54:55] offset:2560 nt
	s_waitcnt vmcnt(23)
	v_cvt_pk_f16_f32 v4, v16, v17
	v_cvt_pk_f16_f32 v5, v18, v19
	ds_write_b64 v110, v[4:5] offset:4352
	global_load_dwordx4 v[16:19], v2, s[56:57] offset:2560 nt
	s_waitcnt vmcnt(23)
	v_cvt_pk_f16_f32 v4, v20, v21
	v_cvt_pk_f16_f32 v5, v22, v23
	ds_write_b64 v110, v[4:5] offset:6528
	global_load_dwordx4 v[20:23], v2, s[58:59] offset:2560 nt
	s_waitcnt vmcnt(23)
	v_cvt_pk_f16_f32 v4, v24, v25
	v_cvt_pk_f16_f32 v5, v26, v27
	ds_write_b64 v110, v[4:5] offset:8704
	global_load_dwordx4 v[24:27], v2, s[60:61] offset:2560 nt
	s_waitcnt vmcnt(23)
	v_cvt_pk_f16_f32 v4, v28, v29
	v_cvt_pk_f16_f32 v5, v30, v31
	ds_write_b64 v110, v[4:5] offset:10880
	global_load_dwordx4 v[28:31], v2, s[62:63] offset:2560 nt
	s_waitcnt vmcnt(23)
	v_cvt_pk_f16_f32 v4, v32, v33
	v_cvt_pk_f16_f32 v5, v34, v35
	ds_write_b64 v110, v[4:5] offset:13056
	global_load_dwordx4 v[32:35], v2, s[64:65] offset:2560 nt
	s_waitcnt vmcnt(23)
	v_cvt_pk_f16_f32 v4, v36, v37
	v_cvt_pk_f16_f32 v5, v38, v39
	ds_write_b64 v110, v[4:5] offset:15232
	global_load_dwordx4 v[36:39], v2, s[66:67] offset:2560 nt
	s_waitcnt lgkmcnt(0)
	s_barrier
	s_waitcnt vmcnt(23)
	v_cvt_pk_f16_f32 v4, v40, v41
	v_cvt_pk_f16_f32 v5, v42, v43
	ds_write_b64 v111, v[4:5]
	global_load_dwordx4 v[40:43], v2, s[52:53] offset:3072 nt
	s_waitcnt vmcnt(23)
	v_cvt_pk_f16_f32 v4, v44, v45
	v_cvt_pk_f16_f32 v5, v46, v47
	ds_write_b64 v111, v[4:5] offset:2176
	global_load_dwordx4 v[44:47], v2, s[54:55] offset:3072 nt
	s_waitcnt vmcnt(23)
	v_cvt_pk_f16_f32 v4, v48, v49
	v_cvt_pk_f16_f32 v5, v50, v51
	ds_write_b64 v111, v[4:5] offset:4352
	global_load_dwordx4 v[48:51], v2, s[56:57] offset:3072 nt
	s_waitcnt vmcnt(23)
	v_cvt_pk_f16_f32 v4, v52, v53
	v_cvt_pk_f16_f32 v5, v54, v55
	ds_write_b64 v111, v[4:5] offset:6528
	global_load_dwordx4 v[52:55], v2, s[58:59] offset:3072 nt
	s_waitcnt vmcnt(23)
	v_cvt_pk_f16_f32 v4, v56, v57
	v_cvt_pk_f16_f32 v5, v58, v59
	ds_write_b64 v111, v[4:5] offset:8704
	global_load_dwordx4 v[56:59], v2, s[60:61] offset:3072 nt
	s_waitcnt vmcnt(23)
	v_cvt_pk_f16_f32 v4, v60, v61
	v_cvt_pk_f16_f32 v5, v62, v63
	ds_write_b64 v111, v[4:5] offset:10880
	global_load_dwordx4 v[60:63], v2, s[62:63] offset:3072 nt
	s_waitcnt vmcnt(23)
	v_cvt_pk_f16_f32 v4, v64, v65
	v_cvt_pk_f16_f32 v5, v66, v67
	ds_write_b64 v111, v[4:5] offset:13056
	global_load_dwordx4 v[64:67], v2, s[64:65] offset:3072 nt
	s_waitcnt vmcnt(23)
	v_cvt_pk_f16_f32 v4, v68, v69
	v_cvt_pk_f16_f32 v5, v70, v71
	ds_write_b64 v111, v[4:5] offset:15232
	global_load_dwordx4 v[68:71], v2, s[66:67] offset:3072 nt
	s_waitcnt lgkmcnt(0)
	s_barrier
	s_waitcnt vmcnt(23)
	v_cvt_pk_f16_f32 v4, v72, v73
	v_cvt_pk_f16_f32 v5, v74, v75
	ds_write_b64 v112, v[4:5]
	v_mov_b32_e32 v72, 0
	v_mov_b32_e32 v73, 0
	v_mov_b32_e32 v74, 0
	v_mov_b32_e32 v75, 0
	s_mov_b64 s[70:71], exec
	s_mov_b64 exec, s[68:69]
	global_load_dwordx4 v[72:75], v2, s[52:53] offset:3584 nt
	s_mov_b64 exec, s[70:71]
	s_waitcnt vmcnt(23)
	v_cvt_pk_f16_f32 v4, v76, v77
	v_cvt_pk_f16_f32 v5, v78, v79
	ds_write_b64 v112, v[4:5] offset:2176
	v_mov_b32_e32 v76, 0
	v_mov_b32_e32 v77, 0
	v_mov_b32_e32 v78, 0
	v_mov_b32_e32 v79, 0
	s_mov_b64 s[70:71], exec
	s_mov_b64 exec, s[68:69]
	global_load_dwordx4 v[76:79], v2, s[54:55] offset:3584 nt
	s_mov_b64 exec, s[70:71]
	s_waitcnt vmcnt(23)
	v_cvt_pk_f16_f32 v4, v80, v81
	v_cvt_pk_f16_f32 v5, v82, v83
	ds_write_b64 v112, v[4:5] offset:4352
	v_mov_b32_e32 v80, 0
	v_mov_b32_e32 v81, 0
	v_mov_b32_e32 v82, 0
	v_mov_b32_e32 v83, 0
	s_mov_b64 s[70:71], exec
	s_mov_b64 exec, s[68:69]
	global_load_dwordx4 v[80:83], v2, s[56:57] offset:3584 nt
	s_mov_b64 exec, s[70:71]
	s_waitcnt vmcnt(23)
	v_cvt_pk_f16_f32 v4, v84, v85
	v_cvt_pk_f16_f32 v5, v86, v87
	ds_write_b64 v112, v[4:5] offset:6528
	v_mov_b32_e32 v84, 0
	v_mov_b32_e32 v85, 0
	v_mov_b32_e32 v86, 0
	v_mov_b32_e32 v87, 0
	s_mov_b64 s[70:71], exec
	s_mov_b64 exec, s[68:69]
	global_load_dwordx4 v[84:87], v2, s[58:59] offset:3584 nt
	s_mov_b64 exec, s[70:71]
	s_waitcnt vmcnt(23)
	v_cvt_pk_f16_f32 v4, v88, v89
	v_cvt_pk_f16_f32 v5, v90, v91
	ds_write_b64 v112, v[4:5] offset:8704
	v_mov_b32_e32 v88, 0
	v_mov_b32_e32 v89, 0
	v_mov_b32_e32 v90, 0
	v_mov_b32_e32 v91, 0
	s_mov_b64 s[70:71], exec
	s_mov_b64 exec, s[68:69]
	global_load_dwordx4 v[88:91], v2, s[60:61] offset:3584 nt
	s_mov_b64 exec, s[70:71]
	s_waitcnt vmcnt(23)
	v_cvt_pk_f16_f32 v4, v92, v93
	v_cvt_pk_f16_f32 v5, v94, v95
	ds_write_b64 v112, v[4:5] offset:10880
	v_mov_b32_e32 v92, 0
	v_mov_b32_e32 v93, 0
	v_mov_b32_e32 v94, 0
	v_mov_b32_e32 v95, 0
	s_mov_b64 s[70:71], exec
	s_mov_b64 exec, s[68:69]
	global_load_dwordx4 v[92:95], v2, s[62:63] offset:3584 nt
	s_mov_b64 exec, s[70:71]
	s_waitcnt vmcnt(23)
	v_cvt_pk_f16_f32 v4, v96, v97
	v_cvt_pk_f16_f32 v5, v98, v99
	ds_write_b64 v112, v[4:5] offset:13056
	v_mov_b32_e32 v96, 0
	v_mov_b32_e32 v97, 0
	v_mov_b32_e32 v98, 0
	v_mov_b32_e32 v99, 0
	s_mov_b64 s[70:71], exec
	s_mov_b64 exec, s[68:69]
	global_load_dwordx4 v[96:99], v2, s[64:65] offset:3584 nt
	s_mov_b64 exec, s[70:71]
	s_waitcnt vmcnt(23)
	v_cvt_pk_f16_f32 v4, v100, v101
	v_cvt_pk_f16_f32 v5, v102, v103
	ds_write_b64 v112, v[4:5] offset:15232
	v_mov_b32_e32 v100, 0
	v_mov_b32_e32 v101, 0
	v_mov_b32_e32 v102, 0
	v_mov_b32_e32 v103, 0
	s_mov_b64 s[70:71], exec
	s_mov_b64 exec, s[68:69]
	global_load_dwordx4 v[100:103], v2, s[66:67] offset:3584 nt
	s_mov_b64 exec, s[70:71]
	s_waitcnt lgkmcnt(0)
	s_barrier
	s_waitcnt vmcnt(23)
	v_cvt_pk_f16_f32 v4, v8, v9
	v_cvt_pk_f16_f32 v5, v10, v11
	ds_write_b64 v110, v[4:5]
	s_waitcnt vmcnt(22)
	v_cvt_pk_f16_f32 v4, v12, v13
	v_cvt_pk_f16_f32 v5, v14, v15
	ds_write_b64 v110, v[4:5] offset:2176
	s_waitcnt vmcnt(21)
	v_cvt_pk_f16_f32 v4, v16, v17
	v_cvt_pk_f16_f32 v5, v18, v19
	ds_write_b64 v110, v[4:5] offset:4352
	s_waitcnt vmcnt(20)
	v_cvt_pk_f16_f32 v4, v20, v21
	v_cvt_pk_f16_f32 v5, v22, v23
	ds_write_b64 v110, v[4:5] offset:6528
	s_waitcnt vmcnt(19)
	v_cvt_pk_f16_f32 v4, v24, v25
	v_cvt_pk_f16_f32 v5, v26, v27
	ds_write_b64 v110, v[4:5] offset:8704
	s_waitcnt vmcnt(18)
	v_cvt_pk_f16_f32 v4, v28, v29
	v_cvt_pk_f16_f32 v5, v30, v31
	ds_write_b64 v110, v[4:5] offset:10880
	s_waitcnt vmcnt(17)
	v_cvt_pk_f16_f32 v4, v32, v33
	v_cvt_pk_f16_f32 v5, v34, v35
	ds_write_b64 v110, v[4:5] offset:13056
	s_waitcnt vmcnt(16)
	v_cvt_pk_f16_f32 v4, v36, v37
	v_cvt_pk_f16_f32 v5, v38, v39
	ds_write_b64 v110, v[4:5] offset:15232
	s_waitcnt lgkmcnt(0)
	s_barrier
	s_waitcnt vmcnt(15)
	v_cvt_pk_f16_f32 v4, v40, v41
	v_cvt_pk_f16_f32 v5, v42, v43
	ds_write_b64 v111, v[4:5]
	s_waitcnt vmcnt(14)
	v_cvt_pk_f16_f32 v4, v44, v45
	v_cvt_pk_f16_f32 v5, v46, v47
	ds_write_b64 v111, v[4:5] offset:2176
	s_waitcnt vmcnt(13)
	v_cvt_pk_f16_f32 v4, v48, v49
	v_cvt_pk_f16_f32 v5, v50, v51
	ds_write_b64 v111, v[4:5] offset:4352
	s_waitcnt vmcnt(12)
	v_cvt_pk_f16_f32 v4, v52, v53
	v_cvt_pk_f16_f32 v5, v54, v55
	ds_write_b64 v111, v[4:5] offset:6528
	s_waitcnt vmcnt(11)
	v_cvt_pk_f16_f32 v4, v56, v57
	v_cvt_pk_f16_f32 v5, v58, v59
	ds_write_b64 v111, v[4:5] offset:8704
	s_waitcnt vmcnt(10)
	v_cvt_pk_f16_f32 v4, v60, v61
	v_cvt_pk_f16_f32 v5, v62, v63
	ds_write_b64 v111, v[4:5] offset:10880
	s_waitcnt vmcnt(9)
	v_cvt_pk_f16_f32 v4, v64, v65
	v_cvt_pk_f16_f32 v5, v66, v67
	ds_write_b64 v111, v[4:5] offset:13056
	s_waitcnt vmcnt(8)
	v_cvt_pk_f16_f32 v4, v68, v69
	v_cvt_pk_f16_f32 v5, v70, v71
	ds_write_b64 v111, v[4:5] offset:15232
	s_waitcnt lgkmcnt(0)
	s_barrier
	s_waitcnt vmcnt(7)
	v_cvt_pk_f16_f32 v4, v72, v73
	v_cvt_pk_f16_f32 v5, v74, v75
	s_mov_b64 s[70:71], exec
	s_mov_b64 exec, s[78:79]
	ds_write_b64 v112, v[4:5]
	s_mov_b64 exec, s[70:71]
	s_waitcnt vmcnt(6)
	v_cvt_pk_f16_f32 v4, v76, v77
	v_cvt_pk_f16_f32 v5, v78, v79
	s_mov_b64 s[70:71], exec
	s_mov_b64 exec, s[78:79]
	ds_write_b64 v112, v[4:5] offset:2176
	s_mov_b64 exec, s[70:71]
	s_waitcnt vmcnt(5)
	v_cvt_pk_f16_f32 v4, v80, v81
	v_cvt_pk_f16_f32 v5, v82, v83
	s_mov_b64 s[70:71], exec
	s_mov_b64 exec, s[78:79]
	ds_write_b64 v112, v[4:5] offset:4352
	s_mov_b64 exec, s[70:71]
	s_waitcnt vmcnt(4)
	v_cvt_pk_f16_f32 v4, v84, v85
	v_cvt_pk_f16_f32 v5, v86, v87
	s_mov_b64 s[70:71], exec
	s_mov_b64 exec, s[78:79]
	ds_write_b64 v112, v[4:5] offset:6528
	s_mov_b64 exec, s[70:71]
	s_waitcnt vmcnt(3)
	v_cvt_pk_f16_f32 v4, v88, v89
	v_cvt_pk_f16_f32 v5, v90, v91
	s_mov_b64 s[70:71], exec
	s_mov_b64 exec, s[78:79]
	ds_write_b64 v112, v[4:5] offset:8704
	s_mov_b64 exec, s[70:71]
	s_waitcnt vmcnt(2)
	v_cvt_pk_f16_f32 v4, v92, v93
	v_cvt_pk_f16_f32 v5, v94, v95
	s_mov_b64 s[70:71], exec
	s_mov_b64 exec, s[78:79]
	ds_write_b64 v112, v[4:5] offset:10880
	s_mov_b64 exec, s[70:71]
	s_waitcnt vmcnt(1)
	v_cvt_pk_f16_f32 v4, v96, v97
	v_cvt_pk_f16_f32 v5, v98, v99
	s_mov_b64 s[70:71], exec
	s_mov_b64 exec, s[78:79]
	ds_write_b64 v112, v[4:5] offset:13056
	s_mov_b64 exec, s[70:71]
	s_waitcnt vmcnt(0)
	v_cvt_pk_f16_f32 v4, v100, v101
	v_cvt_pk_f16_f32 v5, v102, v103
	s_mov_b64 s[70:71], exec
	s_mov_b64 exec, s[78:79]
	ds_write_b64 v112, v[4:5] offset:15232
	s_mov_b64 exec, s[70:71]
	s_waitcnt lgkmcnt(0)
	s_barrier
	s_barrier
	s_barrier
	s_endpgm
